# baseline (speedup 1.0000x reference)
_Z12k1_colsum_q8PKfPjPfS2_:
	s_load_dwordx8 s[4:11], s[0:1], 0x0
	v_and_b32_e32 v1, 63, v0
	v_lshrrev_b32_e32 v41, 6, v0
	s_lshl_b32 s12, s2, 3
	s_nop 0
	v_readfirstlane_b32 s14, v41
	s_add_u32 s12, s12, s14
	s_cmp_lt_u32 s12, 0x6a0
	s_cselect_b32 s29, 1, 0
	v_lshlrev_b32_e32 v34, 4, v1
	v_min_u32_e32 v35, 57, v1
	v_lshlrev_b32_e32 v35, 4, v35
	v_cmp_gt_u32_e64 s[18:19], 58, v1
	s_lshl_b32 s35, s14, 13
	s_add_u32 s36, s35, 0x1000
	v_add_u32_e32 v38, s35, v34
	v_lshrrev_b32_e32 v41, 5, v1
	v_mov_b32_e32 v42, 0xc35000
	v_mul_lo_u32 v39, v41, v42
	v_and_b32_e32 v42, 31, v1
	v_lshl_add_u32 v39, v42, 2, v39
	v_mov_b32_e32 v2, 0
	v_mov_b32_e32 v3, 0
	v_mov_b32_e32 v4, 0
	v_mov_b32_e32 v5, 0
	v_mov_b32_e32 v6, 0
	v_mov_b32_e32 v7, 0
	v_mov_b32_e32 v8, 0
	v_mov_b32_e32 v9, 0
	v_mov_b32_e32 v10, 0
	v_mov_b32_e32 v11, 0
	v_mov_b32_e32 v12, 0
	v_mov_b32_e32 v13, 0
	v_mov_b32_e32 v14, 0
	v_mov_b32_e32 v15, 0
	v_mov_b32_e32 v16, 0
	v_mov_b32_e32 v17, 0
	v_mov_b32_e32 v40, 0
	v_mov_b32_e32 v47, 0x42fe0000
	s_mov_b32 s32, 0x42fe0000
	s_mov_b32 s33, 0xc0c0400
	s_mov_b32 s34, 0x4000c0c
	s_mov_b32 s15, s12
	s_mul_i32 s37, s15, 0xfa0
	s_lshl_b32 s15, s15, 7
	s_waitcnt lgkmcnt(0)
	s_add_u32 s16, s4, s37
	s_addc_u32 s17, s5, 0
	s_add_u32 s40, s6, s15
	s_addc_u32 s41, s7, 0
	s_add_u32 s20, s40, 0
	s_addc_u32 s21, s41, 0
	s_add_u32 s22, s20, 0x186a000
	s_addc_u32 s23, s21, 0
	s_add_u32 s24, s22, 0x186a000
	s_addc_u32 s25, s23, 0
	s_add_u32 s26, s24, 0x186a000
	s_addc_u32 s27, s25, 0
	s_mov_b32 m0, s35
	s_nop 0
	global_load_lds_dwordx4 v34, s[16:17] nt
	global_load_lds_dwordx4 v34, s[16:17] offset:1024 nt
	global_load_lds_dwordx4 v34, s[16:17] offset:2048 nt
	global_load_lds_dwordx4 v35, s[16:17] offset:3072 nt
	s_add_u32 s16, s16, 0xfa0000
	s_addc_u32 s17, s17, 0
	s_waitcnt vmcnt(0)
	ds_read_b128 v[18:21], v38 offset:0
	ds_read_b128 v[22:25], v38 offset:1024
	ds_read_b128 v[26:29], v38 offset:2048
	ds_read_b128 v[30:33], v38 offset:3072
	s_waitcnt lgkmcnt(0)
	s_mov_b32 m0, s36
	s_nop 0
	global_load_lds_dwordx4 v34, s[16:17] nt
	global_load_lds_dwordx4 v34, s[16:17] offset:1024 nt
	global_load_lds_dwordx4 v34, s[16:17] offset:2048 nt
	global_load_lds_dwordx4 v35, s[16:17] offset:3072 nt
	s_add_u32 s16, s16, 0xfa0000
	s_addc_u32 s17, s17, 0
	v_cndmask_b32_e64 v30, 0, v30, s[18:19]
	v_cndmask_b32_e64 v31, 0, v31, s[18:19]
	v_cndmask_b32_e64 v32, 0, v32, s[18:19]
	v_cndmask_b32_e64 v33, 0, v33, s[18:19]
	v_max3_f32 v41, |v18|, |v19|, |v20|
	v_max3_f32 v42, |v21|, |v22|, |v23|
	v_max3_f32 v43, |v24|, |v25|, |v26|
	v_max3_f32 v44, |v27|, |v28|, |v29|
	v_max3_f32 v48, |v30|, |v31|, |v32|
	v_max3_f32 v41, v41, v42, |v33|
	v_max3_f32 v43, v43, v44, v48
	v_max_f32_e32 v41, v41, v43
	v_pk_add_f32 v[2:3], v[2:3], v[18:19]
	v_pk_add_f32 v[4:5], v[4:5], v[20:21]
	v_max_f32_dpp v41, v41, v41 quad_perm:[1,0,3,2] row_mask:0xf bank_mask:0xf
	v_pk_add_f32 v[6:7], v[6:7], v[22:23]
	v_pk_add_f32 v[8:9], v[8:9], v[24:25]
	v_max_f32_dpp v41, v41, v41 quad_perm:[2,3,0,1] row_mask:0xf bank_mask:0xf
	v_pk_add_f32 v[10:11], v[10:11], v[26:27]
	v_pk_add_f32 v[12:13], v[12:13], v[28:29]
	v_max_f32_dpp v41, v41, v41 row_half_mirror row_mask:0xf bank_mask:0xf
	v_pk_add_f32 v[14:15], v[14:15], v[30:31]
	v_pk_add_f32 v[16:17], v[16:17], v[32:33]
	v_max_f32_dpp v41, v41, v41 row_mirror row_mask:0xf bank_mask:0xf
	s_nop 1
	v_max_f32_dpp v41, v41, v41 row_bcast:15 row_mask:0xa bank_mask:0xf
	s_nop 1
	v_max_f32_dpp v41, v41, v41 row_bcast:31 row_mask:0xc bank_mask:0xf
	s_nop 1
	v_readlane_b32 s28, v41, 63
	s_nop 1
	v_div_scale_f32 v48, s[30:31], s28, s28, v47
	v_rcp_f32_e32 v49, v48
	s_nop 0
	v_fma_f32 v50, -v48, v49, 1.0
	v_fmac_f32_e32 v49, v50, v49
	v_mov_b32_e32 v50, s28
	v_div_scale_f32 v50, vcc, s32, v50, s32
	v_mul_f32_e32 v51, v50, v49
	v_fma_f32 v52, -v48, v51, v50
	v_fmac_f32_e32 v51, v52, v49
	v_fma_f32 v48, -v48, v51, v50
	v_div_fmas_f32 v48, v48, v49, v51
	v_div_fixup_f32 v48, v48, s28, v47
	v_cmp_gt_f32_e64 vcc, s28, 0
	v_writelane_b32 v40, s28, 0
	s_nop 0
	v_cndmask_b32_e32 v48, 0, v48, vcc
	v_fmaak_f32 v49, v18, v48, 0x4b400000
	v_fmaak_f32 v50, v19, v48, 0x4b400000
	v_fmaak_f32 v51, v20, v48, 0x4b400000
	v_fmaak_f32 v52, v21, v48, 0x4b400000
	v_perm_b32 v49, v50, v49, s33
	v_perm_b32 v51, v52, v51, s34
	v_or_b32_e32 v56, v49, v51
	v_fmaak_f32 v41, v22, v48, 0x4b400000
	v_fmaak_f32 v42, v23, v48, 0x4b400000
	v_fmaak_f32 v43, v24, v48, 0x4b400000
	v_fmaak_f32 v44, v25, v48, 0x4b400000
	v_perm_b32 v41, v42, v41, s33
	v_perm_b32 v43, v44, v43, s34
	v_or_b32_e32 v57, v41, v43
	v_fmaak_f32 v49, v26, v48, 0x4b400000
	v_fmaak_f32 v50, v27, v48, 0x4b400000
	v_fmaak_f32 v51, v28, v48, 0x4b400000
	v_fmaak_f32 v52, v29, v48, 0x4b400000
	v_perm_b32 v49, v50, v49, s33
	v_perm_b32 v51, v52, v51, s34
	v_or_b32_e32 v58, v49, v51
	v_fmaak_f32 v41, v30, v48, 0x4b400000
	v_fmaak_f32 v42, v31, v48, 0x4b400000
	v_fmaak_f32 v43, v32, v48, 0x4b400000
	v_fmaak_f32 v44, v33, v48, 0x4b400000
	v_perm_b32 v41, v42, v41, s33
	v_perm_b32 v43, v44, v43, s34
	v_or_b32_e32 v59, v41, v43
	s_waitcnt vmcnt(0)
	ds_read_b128 v[18:21], v38 offset:4096
	ds_read_b128 v[22:25], v38 offset:5120
	ds_read_b128 v[26:29], v38 offset:6144
	ds_read_b128 v[30:33], v38 offset:7168
	s_waitcnt lgkmcnt(0)
	s_mov_b32 m0, s35
	s_nop 0
	global_load_lds_dwordx4 v34, s[16:17] nt
	global_load_lds_dwordx4 v34, s[16:17] offset:1024 nt
	global_load_lds_dwordx4 v34, s[16:17] offset:2048 nt
	global_load_lds_dwordx4 v35, s[16:17] offset:3072 nt
	s_add_u32 s16, s16, 0xfa0000
	s_addc_u32 s17, s17, 0
	v_cndmask_b32_e64 v30, 0, v30, s[18:19]
	v_cndmask_b32_e64 v31, 0, v31, s[18:19]
	v_cndmask_b32_e64 v32, 0, v32, s[18:19]
	v_cndmask_b32_e64 v33, 0, v33, s[18:19]
	v_max3_f32 v41, |v18|, |v19|, |v20|
	v_max3_f32 v42, |v21|, |v22|, |v23|
	v_max3_f32 v43, |v24|, |v25|, |v26|
	v_max3_f32 v44, |v27|, |v28|, |v29|
	v_max3_f32 v48, |v30|, |v31|, |v32|
	v_max3_f32 v41, v41, v42, |v33|
	v_max3_f32 v43, v43, v44, v48
	v_max_f32_e32 v41, v41, v43
	v_pk_add_f32 v[2:3], v[2:3], v[18:19]
	v_pk_add_f32 v[4:5], v[4:5], v[20:21]
	v_max_f32_dpp v41, v41, v41 quad_perm:[1,0,3,2] row_mask:0xf bank_mask:0xf
	v_pk_add_f32 v[6:7], v[6:7], v[22:23]
	v_pk_add_f32 v[8:9], v[8:9], v[24:25]
	v_max_f32_dpp v41, v41, v41 quad_perm:[2,3,0,1] row_mask:0xf bank_mask:0xf
	v_pk_add_f32 v[10:11], v[10:11], v[26:27]
	v_pk_add_f32 v[12:13], v[12:13], v[28:29]
	v_max_f32_dpp v41, v41, v41 row_half_mirror row_mask:0xf bank_mask:0xf
	v_pk_add_f32 v[14:15], v[14:15], v[30:31]
	v_pk_add_f32 v[16:17], v[16:17], v[32:33]
	v_max_f32_dpp v41, v41, v41 row_mirror row_mask:0xf bank_mask:0xf
	s_nop 1
	v_max_f32_dpp v41, v41, v41 row_bcast:15 row_mask:0xa bank_mask:0xf
	s_nop 1
	v_max_f32_dpp v41, v41, v41 row_bcast:31 row_mask:0xc bank_mask:0xf
	s_nop 1
	v_readlane_b32 s28, v41, 63
	s_nop 1
	v_div_scale_f32 v48, s[30:31], s28, s28, v47
	v_rcp_f32_e32 v49, v48
	s_nop 0
	v_fma_f32 v50, -v48, v49, 1.0
	v_fmac_f32_e32 v49, v50, v49
	v_mov_b32_e32 v50, s28
	v_div_scale_f32 v50, vcc, s32, v50, s32
	v_mul_f32_e32 v51, v50, v49
	v_fma_f32 v52, -v48, v51, v50
	v_fmac_f32_e32 v51, v52, v49
	v_fma_f32 v48, -v48, v51, v50
	v_div_fmas_f32 v48, v48, v49, v51
	v_div_fixup_f32 v48, v48, s28, v47
	v_cmp_gt_f32_e64 vcc, s28, 0
	v_writelane_b32 v40, s28, 1
	s_nop 0
	v_cndmask_b32_e32 v48, 0, v48, vcc
	v_fmaak_f32 v49, v18, v48, 0x4b400000
	v_fmaak_f32 v50, v19, v48, 0x4b400000
	v_fmaak_f32 v51, v20, v48, 0x4b400000
	v_fmaak_f32 v52, v21, v48, 0x4b400000
	v_perm_b32 v49, v50, v49, s33
	v_perm_b32 v51, v52, v51, s34
	v_or_b32_e32 v60, v49, v51
	v_fmaak_f32 v41, v22, v48, 0x4b400000
	v_fmaak_f32 v42, v23, v48, 0x4b400000
	v_fmaak_f32 v43, v24, v48, 0x4b400000
	v_fmaak_f32 v44, v25, v48, 0x4b400000
	v_perm_b32 v41, v42, v41, s33
	v_perm_b32 v43, v44, v43, s34
	v_or_b32_e32 v61, v41, v43
	v_fmaak_f32 v49, v26, v48, 0x4b400000
	v_fmaak_f32 v50, v27, v48, 0x4b400000
	v_fmaak_f32 v51, v28, v48, 0x4b400000
	v_fmaak_f32 v52, v29, v48, 0x4b400000
	v_perm_b32 v49, v50, v49, s33
	v_perm_b32 v51, v52, v51, s34
	v_or_b32_e32 v62, v49, v51
	v_fmaak_f32 v41, v30, v48, 0x4b400000
	v_fmaak_f32 v42, v31, v48, 0x4b400000
	v_fmaak_f32 v43, v32, v48, 0x4b400000
	v_fmaak_f32 v44, v33, v48, 0x4b400000
	v_perm_b32 v41, v42, v41, s33
	v_perm_b32 v43, v44, v43, s34
	v_or_b32_e32 v63, v41, v43
	s_waitcnt vmcnt(0)
	ds_read_b128 v[18:21], v38 offset:0
	ds_read_b128 v[22:25], v38 offset:1024
	ds_read_b128 v[26:29], v38 offset:2048
	ds_read_b128 v[30:33], v38 offset:3072
	s_waitcnt lgkmcnt(0)
	s_mov_b32 m0, s36
	s_nop 0
	global_load_lds_dwordx4 v34, s[16:17] nt
	global_load_lds_dwordx4 v34, s[16:17] offset:1024 nt
	global_load_lds_dwordx4 v34, s[16:17] offset:2048 nt
	global_load_lds_dwordx4 v35, s[16:17] offset:3072 nt
	s_add_u32 s16, s16, 0xfa0000
	s_addc_u32 s17, s17, 0
	v_cndmask_b32_e64 v30, 0, v30, s[18:19]
	v_cndmask_b32_e64 v31, 0, v31, s[18:19]
	v_cndmask_b32_e64 v32, 0, v32, s[18:19]
	v_cndmask_b32_e64 v33, 0, v33, s[18:19]
	v_max3_f32 v41, |v18|, |v19|, |v20|
	v_max3_f32 v42, |v21|, |v22|, |v23|
	v_max3_f32 v43, |v24|, |v25|, |v26|
	v_max3_f32 v44, |v27|, |v28|, |v29|
	v_max3_f32 v48, |v30|, |v31|, |v32|
	v_max3_f32 v41, v41, v42, |v33|
	v_max3_f32 v43, v43, v44, v48
	v_max_f32_e32 v41, v41, v43
	v_pk_add_f32 v[2:3], v[2:3], v[18:19]
	v_pk_add_f32 v[4:5], v[4:5], v[20:21]
	v_max_f32_dpp v41, v41, v41 quad_perm:[1,0,3,2] row_mask:0xf bank_mask:0xf
	v_pk_add_f32 v[6:7], v[6:7], v[22:23]
	v_pk_add_f32 v[8:9], v[8:9], v[24:25]
	v_max_f32_dpp v41, v41, v41 quad_perm:[2,3,0,1] row_mask:0xf bank_mask:0xf
	v_pk_add_f32 v[10:11], v[10:11], v[26:27]
	v_pk_add_f32 v[12:13], v[12:13], v[28:29]
	v_max_f32_dpp v41, v41, v41 row_half_mirror row_mask:0xf bank_mask:0xf
	v_pk_add_f32 v[14:15], v[14:15], v[30:31]
	v_pk_add_f32 v[16:17], v[16:17], v[32:33]
	v_max_f32_dpp v41, v41, v41 row_mirror row_mask:0xf bank_mask:0xf
	s_nop 1
	v_max_f32_dpp v41, v41, v41 row_bcast:15 row_mask:0xa bank_mask:0xf
	s_nop 1
	v_max_f32_dpp v41, v41, v41 row_bcast:31 row_mask:0xc bank_mask:0xf
	s_nop 1
	v_readlane_b32 s28, v41, 63
	s_nop 1
	v_div_scale_f32 v48, s[30:31], s28, s28, v47
	v_rcp_f32_e32 v49, v48
	s_nop 0
	v_fma_f32 v50, -v48, v49, 1.0
	v_fmac_f32_e32 v49, v50, v49
	v_mov_b32_e32 v50, s28
	v_div_scale_f32 v50, vcc, s32, v50, s32
	v_mul_f32_e32 v51, v50, v49
	v_fma_f32 v52, -v48, v51, v50
	v_fmac_f32_e32 v51, v52, v49
	v_fma_f32 v48, -v48, v51, v50
	v_div_fmas_f32 v48, v48, v49, v51
	v_div_fixup_f32 v48, v48, s28, v47
	v_cmp_gt_f32_e64 vcc, s28, 0
	v_writelane_b32 v40, s28, 2
	s_nop 0
	v_cndmask_b32_e32 v48, 0, v48, vcc
	v_fmaak_f32 v49, v18, v48, 0x4b400000
	v_fmaak_f32 v50, v19, v48, 0x4b400000
	v_fmaak_f32 v51, v20, v48, 0x4b400000
	v_fmaak_f32 v52, v21, v48, 0x4b400000
	v_perm_b32 v49, v50, v49, s33
	v_perm_b32 v51, v52, v51, s34
	v_or_b32_e32 v64, v49, v51
	v_fmaak_f32 v41, v22, v48, 0x4b400000
	v_fmaak_f32 v42, v23, v48, 0x4b400000
	v_fmaak_f32 v43, v24, v48, 0x4b400000
	v_fmaak_f32 v44, v25, v48, 0x4b400000
	v_perm_b32 v41, v42, v41, s33
	v_perm_b32 v43, v44, v43, s34
	v_or_b32_e32 v65, v41, v43
	v_fmaak_f32 v49, v26, v48, 0x4b400000
	v_fmaak_f32 v50, v27, v48, 0x4b400000
	v_fmaak_f32 v51, v28, v48, 0x4b400000
	v_fmaak_f32 v52, v29, v48, 0x4b400000
	v_perm_b32 v49, v50, v49, s33
	v_perm_b32 v51, v52, v51, s34
	v_or_b32_e32 v66, v49, v51
	v_fmaak_f32 v41, v30, v48, 0x4b400000
	v_fmaak_f32 v42, v31, v48, 0x4b400000
	v_fmaak_f32 v43, v32, v48, 0x4b400000
	v_fmaak_f32 v44, v33, v48, 0x4b400000
	v_perm_b32 v41, v42, v41, s33
	v_perm_b32 v43, v44, v43, s34
	v_or_b32_e32 v67, v41, v43
	s_waitcnt vmcnt(0)
	ds_read_b128 v[18:21], v38 offset:4096
	ds_read_b128 v[22:25], v38 offset:5120
	ds_read_b128 v[26:29], v38 offset:6144
	ds_read_b128 v[30:33], v38 offset:7168
	s_waitcnt lgkmcnt(0)
	s_mov_b32 m0, s35
	s_nop 0
	global_load_lds_dwordx4 v34, s[16:17] nt
	global_load_lds_dwordx4 v34, s[16:17] offset:1024 nt
	global_load_lds_dwordx4 v34, s[16:17] offset:2048 nt
	global_load_lds_dwordx4 v35, s[16:17] offset:3072 nt
	s_add_u32 s16, s16, 0xfa0000
	s_addc_u32 s17, s17, 0
	v_cndmask_b32_e64 v30, 0, v30, s[18:19]
	v_cndmask_b32_e64 v31, 0, v31, s[18:19]
	v_cndmask_b32_e64 v32, 0, v32, s[18:19]
	v_cndmask_b32_e64 v33, 0, v33, s[18:19]
	v_max3_f32 v41, |v18|, |v19|, |v20|
	v_max3_f32 v42, |v21|, |v22|, |v23|
	v_max3_f32 v43, |v24|, |v25|, |v26|
	v_max3_f32 v44, |v27|, |v28|, |v29|
	v_max3_f32 v48, |v30|, |v31|, |v32|
	v_max3_f32 v41, v41, v42, |v33|
	v_max3_f32 v43, v43, v44, v48
	v_max_f32_e32 v41, v41, v43
	v_pk_add_f32 v[2:3], v[2:3], v[18:19]
	v_pk_add_f32 v[4:5], v[4:5], v[20:21]
	v_max_f32_dpp v41, v41, v41 quad_perm:[1,0,3,2] row_mask:0xf bank_mask:0xf
	v_pk_add_f32 v[6:7], v[6:7], v[22:23]
	v_pk_add_f32 v[8:9], v[8:9], v[24:25]
	v_max_f32_dpp v41, v41, v41 quad_perm:[2,3,0,1] row_mask:0xf bank_mask:0xf
	v_pk_add_f32 v[10:11], v[10:11], v[26:27]
	v_pk_add_f32 v[12:13], v[12:13], v[28:29]
	v_max_f32_dpp v41, v41, v41 row_half_mirror row_mask:0xf bank_mask:0xf
	v_pk_add_f32 v[14:15], v[14:15], v[30:31]
	v_pk_add_f32 v[16:17], v[16:17], v[32:33]
	v_max_f32_dpp v41, v41, v41 row_mirror row_mask:0xf bank_mask:0xf
	s_nop 1
	v_max_f32_dpp v41, v41, v41 row_bcast:15 row_mask:0xa bank_mask:0xf
	s_nop 1
	v_max_f32_dpp v41, v41, v41 row_bcast:31 row_mask:0xc bank_mask:0xf
	s_nop 1
	v_readlane_b32 s28, v41, 63
	s_nop 1
	v_div_scale_f32 v48, s[30:31], s28, s28, v47
	v_rcp_f32_e32 v49, v48
	s_nop 0
	v_fma_f32 v50, -v48, v49, 1.0
	v_fmac_f32_e32 v49, v50, v49
	v_mov_b32_e32 v50, s28
	v_div_scale_f32 v50, vcc, s32, v50, s32
	v_mul_f32_e32 v51, v50, v49
	v_fma_f32 v52, -v48, v51, v50
	v_fmac_f32_e32 v51, v52, v49
	v_fma_f32 v48, -v48, v51, v50
	v_div_fmas_f32 v48, v48, v49, v51
	v_div_fixup_f32 v48, v48, s28, v47
	v_cmp_gt_f32_e64 vcc, s28, 0
	v_writelane_b32 v40, s28, 3
	s_nop 0
	v_cndmask_b32_e32 v48, 0, v48, vcc
	v_fmaak_f32 v49, v18, v48, 0x4b400000
	v_fmaak_f32 v50, v19, v48, 0x4b400000
	v_fmaak_f32 v51, v20, v48, 0x4b400000
	v_fmaak_f32 v52, v21, v48, 0x4b400000
	v_perm_b32 v49, v50, v49, s33
	v_perm_b32 v51, v52, v51, s34
	v_or_b32_e32 v68, v49, v51
	v_fmaak_f32 v41, v22, v48, 0x4b400000
	v_fmaak_f32 v42, v23, v48, 0x4b400000
	v_fmaak_f32 v43, v24, v48, 0x4b400000
	v_fmaak_f32 v44, v25, v48, 0x4b400000
	v_perm_b32 v41, v42, v41, s33
	v_perm_b32 v43, v44, v43, s34
	v_or_b32_e32 v69, v41, v43
	v_fmaak_f32 v49, v26, v48, 0x4b400000
	v_fmaak_f32 v50, v27, v48, 0x4b400000
	v_fmaak_f32 v51, v28, v48, 0x4b400000
	v_fmaak_f32 v52, v29, v48, 0x4b400000
	v_perm_b32 v49, v50, v49, s33
	v_perm_b32 v51, v52, v51, s34
	v_or_b32_e32 v70, v49, v51
	v_fmaak_f32 v41, v30, v48, 0x4b400000
	v_fmaak_f32 v42, v31, v48, 0x4b400000
	v_fmaak_f32 v43, v32, v48, 0x4b400000
	v_fmaak_f32 v44, v33, v48, 0x4b400000
	v_perm_b32 v41, v42, v41, s33
	v_perm_b32 v43, v44, v43, s34
	v_or_b32_e32 v71, v41, v43
	s_waitcnt vmcnt(0)
	ds_read_b128 v[18:21], v38 offset:0
	ds_read_b128 v[22:25], v38 offset:1024
	ds_read_b128 v[26:29], v38 offset:2048
	ds_read_b128 v[30:33], v38 offset:3072
	s_waitcnt lgkmcnt(0)
	s_mov_b32 m0, s36
	s_nop 0
	global_load_lds_dwordx4 v34, s[16:17] nt
	global_load_lds_dwordx4 v34, s[16:17] offset:1024 nt
	global_load_lds_dwordx4 v34, s[16:17] offset:2048 nt
	global_load_lds_dwordx4 v35, s[16:17] offset:3072 nt
	s_add_u32 s16, s16, 0xfa0000
	s_addc_u32 s17, s17, 0
	v_cndmask_b32_e64 v30, 0, v30, s[18:19]
	v_cndmask_b32_e64 v31, 0, v31, s[18:19]
	v_cndmask_b32_e64 v32, 0, v32, s[18:19]
	v_cndmask_b32_e64 v33, 0, v33, s[18:19]
	v_max3_f32 v41, |v18|, |v19|, |v20|
	v_max3_f32 v42, |v21|, |v22|, |v23|
	v_max3_f32 v43, |v24|, |v25|, |v26|
	v_max3_f32 v44, |v27|, |v28|, |v29|
	v_max3_f32 v48, |v30|, |v31|, |v32|
	v_max3_f32 v41, v41, v42, |v33|
	v_max3_f32 v43, v43, v44, v48
	v_max_f32_e32 v41, v41, v43
	v_pk_add_f32 v[2:3], v[2:3], v[18:19]
	v_pk_add_f32 v[4:5], v[4:5], v[20:21]
	v_max_f32_dpp v41, v41, v41 quad_perm:[1,0,3,2] row_mask:0xf bank_mask:0xf
	v_pk_add_f32 v[6:7], v[6:7], v[22:23]
	v_pk_add_f32 v[8:9], v[8:9], v[24:25]
	v_max_f32_dpp v41, v41, v41 quad_perm:[2,3,0,1] row_mask:0xf bank_mask:0xf
	v_pk_add_f32 v[10:11], v[10:11], v[26:27]
	v_pk_add_f32 v[12:13], v[12:13], v[28:29]
	v_max_f32_dpp v41, v41, v41 row_half_mirror row_mask:0xf bank_mask:0xf
	v_pk_add_f32 v[14:15], v[14:15], v[30:31]
	v_pk_add_f32 v[16:17], v[16:17], v[32:33]
	v_max_f32_dpp v41, v41, v41 row_mirror row_mask:0xf bank_mask:0xf
	s_nop 1
	v_max_f32_dpp v41, v41, v41 row_bcast:15 row_mask:0xa bank_mask:0xf
	s_nop 1
	v_max_f32_dpp v41, v41, v41 row_bcast:31 row_mask:0xc bank_mask:0xf
	s_nop 1
	v_readlane_b32 s28, v41, 63
	s_nop 1
	v_div_scale_f32 v48, s[30:31], s28, s28, v47
	v_rcp_f32_e32 v49, v48
	s_nop 0
	v_fma_f32 v50, -v48, v49, 1.0
	v_fmac_f32_e32 v49, v50, v49
	v_mov_b32_e32 v50, s28
	v_div_scale_f32 v50, vcc, s32, v50, s32
	v_mul_f32_e32 v51, v50, v49
	v_fma_f32 v52, -v48, v51, v50
	v_fmac_f32_e32 v51, v52, v49
	v_fma_f32 v48, -v48, v51, v50
	v_div_fmas_f32 v48, v48, v49, v51
	v_div_fixup_f32 v48, v48, s28, v47
	v_cmp_gt_f32_e64 vcc, s28, 0
	v_writelane_b32 v40, s28, 4
	s_nop 0
	v_cndmask_b32_e32 v48, 0, v48, vcc
	v_fmaak_f32 v49, v18, v48, 0x4b400000
	v_fmaak_f32 v50, v19, v48, 0x4b400000
	v_fmaak_f32 v51, v20, v48, 0x4b400000
	v_fmaak_f32 v52, v21, v48, 0x4b400000
	v_perm_b32 v49, v50, v49, s33
	v_perm_b32 v51, v52, v51, s34
	v_or_b32_e32 v72, v49, v51
	v_fmaak_f32 v41, v22, v48, 0x4b400000
	v_fmaak_f32 v42, v23, v48, 0x4b400000
	v_fmaak_f32 v43, v24, v48, 0x4b400000
	v_fmaak_f32 v44, v25, v48, 0x4b400000
	v_perm_b32 v41, v42, v41, s33
	v_perm_b32 v43, v44, v43, s34
	v_or_b32_e32 v73, v41, v43
	v_fmaak_f32 v49, v26, v48, 0x4b400000
	v_fmaak_f32 v50, v27, v48, 0x4b400000
	v_fmaak_f32 v51, v28, v48, 0x4b400000
	v_fmaak_f32 v52, v29, v48, 0x4b400000
	v_perm_b32 v49, v50, v49, s33
	v_perm_b32 v51, v52, v51, s34
	v_or_b32_e32 v74, v49, v51
	v_fmaak_f32 v41, v30, v48, 0x4b400000
	v_fmaak_f32 v42, v31, v48, 0x4b400000
	v_fmaak_f32 v43, v32, v48, 0x4b400000
	v_fmaak_f32 v44, v33, v48, 0x4b400000
	v_perm_b32 v41, v42, v41, s33
	v_perm_b32 v43, v44, v43, s34
	v_or_b32_e32 v75, v41, v43
	s_waitcnt vmcnt(0)
	ds_read_b128 v[18:21], v38 offset:4096
	ds_read_b128 v[22:25], v38 offset:5120
	ds_read_b128 v[26:29], v38 offset:6144
	ds_read_b128 v[30:33], v38 offset:7168
	s_waitcnt lgkmcnt(0)
	s_mov_b32 m0, s35
	s_nop 0
	global_load_lds_dwordx4 v34, s[16:17] nt
	global_load_lds_dwordx4 v34, s[16:17] offset:1024 nt
	global_load_lds_dwordx4 v34, s[16:17] offset:2048 nt
	global_load_lds_dwordx4 v35, s[16:17] offset:3072 nt
	s_add_u32 s16, s16, 0xfa0000
	s_addc_u32 s17, s17, 0
	v_cndmask_b32_e64 v30, 0, v30, s[18:19]
	v_cndmask_b32_e64 v31, 0, v31, s[18:19]
	v_cndmask_b32_e64 v32, 0, v32, s[18:19]
	v_cndmask_b32_e64 v33, 0, v33, s[18:19]
	v_max3_f32 v41, |v18|, |v19|, |v20|
	v_max3_f32 v42, |v21|, |v22|, |v23|
	v_max3_f32 v43, |v24|, |v25|, |v26|
	v_max3_f32 v44, |v27|, |v28|, |v29|
	v_max3_f32 v48, |v30|, |v31|, |v32|
	v_max3_f32 v41, v41, v42, |v33|
	v_max3_f32 v43, v43, v44, v48
	v_max_f32_e32 v41, v41, v43
	v_pk_add_f32 v[2:3], v[2:3], v[18:19]
	v_pk_add_f32 v[4:5], v[4:5], v[20:21]
	v_max_f32_dpp v41, v41, v41 quad_perm:[1,0,3,2] row_mask:0xf bank_mask:0xf
	v_pk_add_f32 v[6:7], v[6:7], v[22:23]
	v_pk_add_f32 v[8:9], v[8:9], v[24:25]
	v_max_f32_dpp v41, v41, v41 quad_perm:[2,3,0,1] row_mask:0xf bank_mask:0xf
	v_pk_add_f32 v[10:11], v[10:11], v[26:27]
	v_pk_add_f32 v[12:13], v[12:13], v[28:29]
	v_max_f32_dpp v41, v41, v41 row_half_mirror row_mask:0xf bank_mask:0xf
	v_pk_add_f32 v[14:15], v[14:15], v[30:31]
	v_pk_add_f32 v[16:17], v[16:17], v[32:33]
	v_max_f32_dpp v41, v41, v41 row_mirror row_mask:0xf bank_mask:0xf
	s_nop 1
	v_max_f32_dpp v41, v41, v41 row_bcast:15 row_mask:0xa bank_mask:0xf
	s_nop 1
	v_max_f32_dpp v41, v41, v41 row_bcast:31 row_mask:0xc bank_mask:0xf
	s_nop 1
	v_readlane_b32 s28, v41, 63
	s_nop 1
	v_div_scale_f32 v48, s[30:31], s28, s28, v47
	v_rcp_f32_e32 v49, v48
	s_nop 0
	v_fma_f32 v50, -v48, v49, 1.0
	v_fmac_f32_e32 v49, v50, v49
	v_mov_b32_e32 v50, s28
	v_div_scale_f32 v50, vcc, s32, v50, s32
	v_mul_f32_e32 v51, v50, v49
	v_fma_f32 v52, -v48, v51, v50
	v_fmac_f32_e32 v51, v52, v49
	v_fma_f32 v48, -v48, v51, v50
	v_div_fmas_f32 v48, v48, v49, v51
	v_div_fixup_f32 v48, v48, s28, v47
	v_cmp_gt_f32_e64 vcc, s28, 0
	v_writelane_b32 v40, s28, 5
	s_nop 0
	v_cndmask_b32_e32 v48, 0, v48, vcc
	v_fmaak_f32 v49, v18, v48, 0x4b400000
	v_fmaak_f32 v50, v19, v48, 0x4b400000
	v_fmaak_f32 v51, v20, v48, 0x4b400000
	v_fmaak_f32 v52, v21, v48, 0x4b400000
	v_perm_b32 v49, v50, v49, s33
	v_perm_b32 v51, v52, v51, s34
	v_or_b32_e32 v76, v49, v51
	v_fmaak_f32 v41, v22, v48, 0x4b400000
	v_fmaak_f32 v42, v23, v48, 0x4b400000
	v_fmaak_f32 v43, v24, v48, 0x4b400000
	v_fmaak_f32 v44, v25, v48, 0x4b400000
	v_perm_b32 v41, v42, v41, s33
	v_perm_b32 v43, v44, v43, s34
	v_or_b32_e32 v77, v41, v43
	v_fmaak_f32 v49, v26, v48, 0x4b400000
	v_fmaak_f32 v50, v27, v48, 0x4b400000
	v_fmaak_f32 v51, v28, v48, 0x4b400000
	v_fmaak_f32 v52, v29, v48, 0x4b400000
	v_perm_b32 v49, v50, v49, s33
	v_perm_b32 v51, v52, v51, s34
	v_or_b32_e32 v78, v49, v51
	v_fmaak_f32 v41, v30, v48, 0x4b400000
	v_fmaak_f32 v42, v31, v48, 0x4b400000
	v_fmaak_f32 v43, v32, v48, 0x4b400000
	v_fmaak_f32 v44, v33, v48, 0x4b400000
	v_perm_b32 v41, v42, v41, s33
	v_perm_b32 v43, v44, v43, s34
	v_or_b32_e32 v79, v41, v43
	s_waitcnt vmcnt(0)
	ds_read_b128 v[18:21], v38 offset:0
	ds_read_b128 v[22:25], v38 offset:1024
	ds_read_b128 v[26:29], v38 offset:2048
	ds_read_b128 v[30:33], v38 offset:3072
	s_waitcnt lgkmcnt(0)
	s_mov_b32 m0, s36
	s_nop 0
	global_load_lds_dwordx4 v34, s[16:17] nt
	global_load_lds_dwordx4 v34, s[16:17] offset:1024 nt
	global_load_lds_dwordx4 v34, s[16:17] offset:2048 nt
	global_load_lds_dwordx4 v35, s[16:17] offset:3072 nt
	s_add_u32 s16, s16, 0xfa0000
	s_addc_u32 s17, s17, 0
	v_cndmask_b32_e64 v30, 0, v30, s[18:19]
	v_cndmask_b32_e64 v31, 0, v31, s[18:19]
	v_cndmask_b32_e64 v32, 0, v32, s[18:19]
	v_cndmask_b32_e64 v33, 0, v33, s[18:19]
	v_max3_f32 v41, |v18|, |v19|, |v20|
	v_max3_f32 v42, |v21|, |v22|, |v23|
	v_max3_f32 v43, |v24|, |v25|, |v26|
	v_max3_f32 v44, |v27|, |v28|, |v29|
	v_max3_f32 v48, |v30|, |v31|, |v32|
	v_max3_f32 v41, v41, v42, |v33|
	v_max3_f32 v43, v43, v44, v48
	v_max_f32_e32 v41, v41, v43
	v_pk_add_f32 v[2:3], v[2:3], v[18:19]
	v_pk_add_f32 v[4:5], v[4:5], v[20:21]
	v_max_f32_dpp v41, v41, v41 quad_perm:[1,0,3,2] row_mask:0xf bank_mask:0xf
	v_pk_add_f32 v[6:7], v[6:7], v[22:23]
	v_pk_add_f32 v[8:9], v[8:9], v[24:25]
	v_max_f32_dpp v41, v41, v41 quad_perm:[2,3,0,1] row_mask:0xf bank_mask:0xf
	v_pk_add_f32 v[10:11], v[10:11], v[26:27]
	v_pk_add_f32 v[12:13], v[12:13], v[28:29]
	v_max_f32_dpp v41, v41, v41 row_half_mirror row_mask:0xf bank_mask:0xf
	v_pk_add_f32 v[14:15], v[14:15], v[30:31]
	v_pk_add_f32 v[16:17], v[16:17], v[32:33]
	v_max_f32_dpp v41, v41, v41 row_mirror row_mask:0xf bank_mask:0xf
	s_nop 1
	v_max_f32_dpp v41, v41, v41 row_bcast:15 row_mask:0xa bank_mask:0xf
	s_nop 1
	v_max_f32_dpp v41, v41, v41 row_bcast:31 row_mask:0xc bank_mask:0xf
	s_nop 1
	v_readlane_b32 s28, v41, 63
	s_nop 1
	v_div_scale_f32 v48, s[30:31], s28, s28, v47
	v_rcp_f32_e32 v49, v48
	s_nop 0
	v_fma_f32 v50, -v48, v49, 1.0
	v_fmac_f32_e32 v49, v50, v49
	v_mov_b32_e32 v50, s28
	v_div_scale_f32 v50, vcc, s32, v50, s32
	v_mul_f32_e32 v51, v50, v49
	v_fma_f32 v52, -v48, v51, v50
	v_fmac_f32_e32 v51, v52, v49
	v_fma_f32 v48, -v48, v51, v50
	v_div_fmas_f32 v48, v48, v49, v51
	v_div_fixup_f32 v48, v48, s28, v47
	v_cmp_gt_f32_e64 vcc, s28, 0
	v_writelane_b32 v40, s28, 6
	s_nop 0
	v_cndmask_b32_e32 v48, 0, v48, vcc
	v_fmaak_f32 v49, v18, v48, 0x4b400000
	v_fmaak_f32 v50, v19, v48, 0x4b400000
	v_fmaak_f32 v51, v20, v48, 0x4b400000
	v_fmaak_f32 v52, v21, v48, 0x4b400000
	v_perm_b32 v49, v50, v49, s33
	v_perm_b32 v51, v52, v51, s34
	v_or_b32_e32 v80, v49, v51
	v_fmaak_f32 v41, v22, v48, 0x4b400000
	v_fmaak_f32 v42, v23, v48, 0x4b400000
	v_fmaak_f32 v43, v24, v48, 0x4b400000
	v_fmaak_f32 v44, v25, v48, 0x4b400000
	v_perm_b32 v41, v42, v41, s33
	v_perm_b32 v43, v44, v43, s34
	v_or_b32_e32 v81, v41, v43
	v_fmaak_f32 v49, v26, v48, 0x4b400000
	v_fmaak_f32 v50, v27, v48, 0x4b400000
	v_fmaak_f32 v51, v28, v48, 0x4b400000
	v_fmaak_f32 v52, v29, v48, 0x4b400000
	v_perm_b32 v49, v50, v49, s33
	v_perm_b32 v51, v52, v51, s34
	v_or_b32_e32 v82, v49, v51
	v_fmaak_f32 v41, v30, v48, 0x4b400000
	v_fmaak_f32 v42, v31, v48, 0x4b400000
	v_fmaak_f32 v43, v32, v48, 0x4b400000
	v_fmaak_f32 v44, v33, v48, 0x4b400000
	v_perm_b32 v41, v42, v41, s33
	v_perm_b32 v43, v44, v43, s34
	v_or_b32_e32 v83, v41, v43
	s_waitcnt vmcnt(0)
	ds_read_b128 v[18:21], v38 offset:4096
	ds_read_b128 v[22:25], v38 offset:5120
	ds_read_b128 v[26:29], v38 offset:6144
	ds_read_b128 v[30:33], v38 offset:7168
	s_waitcnt lgkmcnt(0)
	s_mov_b32 m0, s35
	s_nop 0
	global_load_lds_dwordx4 v34, s[16:17] nt
	global_load_lds_dwordx4 v34, s[16:17] offset:1024 nt
	global_load_lds_dwordx4 v34, s[16:17] offset:2048 nt
	global_load_lds_dwordx4 v35, s[16:17] offset:3072 nt
	s_add_u32 s16, s16, 0xfa0000
	s_addc_u32 s17, s17, 0
	v_cndmask_b32_e64 v30, 0, v30, s[18:19]
	v_cndmask_b32_e64 v31, 0, v31, s[18:19]
	v_cndmask_b32_e64 v32, 0, v32, s[18:19]
	v_cndmask_b32_e64 v33, 0, v33, s[18:19]
	v_max3_f32 v41, |v18|, |v19|, |v20|
	v_max3_f32 v42, |v21|, |v22|, |v23|
	v_max3_f32 v43, |v24|, |v25|, |v26|
	v_max3_f32 v44, |v27|, |v28|, |v29|
	v_max3_f32 v48, |v30|, |v31|, |v32|
	v_max3_f32 v41, v41, v42, |v33|
	v_max3_f32 v43, v43, v44, v48
	v_max_f32_e32 v41, v41, v43
	v_pk_add_f32 v[2:3], v[2:3], v[18:19]
	v_pk_add_f32 v[4:5], v[4:5], v[20:21]
	v_max_f32_dpp v41, v41, v41 quad_perm:[1,0,3,2] row_mask:0xf bank_mask:0xf
	v_pk_add_f32 v[6:7], v[6:7], v[22:23]
	v_pk_add_f32 v[8:9], v[8:9], v[24:25]
	v_max_f32_dpp v41, v41, v41 quad_perm:[2,3,0,1] row_mask:0xf bank_mask:0xf
	v_pk_add_f32 v[10:11], v[10:11], v[26:27]
	v_pk_add_f32 v[12:13], v[12:13], v[28:29]
	v_max_f32_dpp v41, v41, v41 row_half_mirror row_mask:0xf bank_mask:0xf
	v_pk_add_f32 v[14:15], v[14:15], v[30:31]
	v_pk_add_f32 v[16:17], v[16:17], v[32:33]
	v_max_f32_dpp v41, v41, v41 row_mirror row_mask:0xf bank_mask:0xf
	s_nop 1
	v_max_f32_dpp v41, v41, v41 row_bcast:15 row_mask:0xa bank_mask:0xf
	s_nop 1
	v_max_f32_dpp v41, v41, v41 row_bcast:31 row_mask:0xc bank_mask:0xf
	s_nop 1
	v_readlane_b32 s28, v41, 63
	s_nop 1
	v_div_scale_f32 v48, s[30:31], s28, s28, v47
	v_rcp_f32_e32 v49, v48
	s_nop 0
	v_fma_f32 v50, -v48, v49, 1.0
	v_fmac_f32_e32 v49, v50, v49
	v_mov_b32_e32 v50, s28
	v_div_scale_f32 v50, vcc, s32, v50, s32
	v_mul_f32_e32 v51, v50, v49
	v_fma_f32 v52, -v48, v51, v50
	v_fmac_f32_e32 v51, v52, v49
	v_fma_f32 v48, -v48, v51, v50
	v_div_fmas_f32 v48, v48, v49, v51
	v_div_fixup_f32 v48, v48, s28, v47
	v_cmp_gt_f32_e64 vcc, s28, 0
	v_writelane_b32 v40, s28, 7
	s_nop 0
	v_cndmask_b32_e32 v48, 0, v48, vcc
	v_fmaak_f32 v49, v18, v48, 0x4b400000
	v_fmaak_f32 v50, v19, v48, 0x4b400000
	v_fmaak_f32 v51, v20, v48, 0x4b400000
	v_fmaak_f32 v52, v21, v48, 0x4b400000
	v_perm_b32 v49, v50, v49, s33
	v_perm_b32 v51, v52, v51, s34
	v_or_b32_e32 v84, v49, v51
	v_fmaak_f32 v41, v22, v48, 0x4b400000
	v_fmaak_f32 v42, v23, v48, 0x4b400000
	v_fmaak_f32 v43, v24, v48, 0x4b400000
	v_fmaak_f32 v44, v25, v48, 0x4b400000
	v_perm_b32 v41, v42, v41, s33
	v_perm_b32 v43, v44, v43, s34
	v_or_b32_e32 v85, v41, v43
	v_fmaak_f32 v49, v26, v48, 0x4b400000
	v_fmaak_f32 v50, v27, v48, 0x4b400000
	v_fmaak_f32 v51, v28, v48, 0x4b400000
	v_fmaak_f32 v52, v29, v48, 0x4b400000
	v_perm_b32 v49, v50, v49, s33
	v_perm_b32 v51, v52, v51, s34
	v_or_b32_e32 v86, v49, v51
	v_fmaak_f32 v41, v30, v48, 0x4b400000
	v_fmaak_f32 v42, v31, v48, 0x4b400000
	v_fmaak_f32 v43, v32, v48, 0x4b400000
	v_fmaak_f32 v44, v33, v48, 0x4b400000
	v_perm_b32 v41, v42, v41, s33
	v_perm_b32 v43, v44, v43, s34
	v_or_b32_e32 v87, v41, v43
	s_waitcnt vmcnt(0)
	ds_read_b128 v[18:21], v38 offset:0
	ds_read_b128 v[22:25], v38 offset:1024
	ds_read_b128 v[26:29], v38 offset:2048
	ds_read_b128 v[30:33], v38 offset:3072
	s_waitcnt lgkmcnt(0)
	s_mov_b32 m0, s36
	s_nop 0
	global_load_lds_dwordx4 v34, s[16:17] nt
	global_load_lds_dwordx4 v34, s[16:17] offset:1024 nt
	global_load_lds_dwordx4 v34, s[16:17] offset:2048 nt
	global_load_lds_dwordx4 v35, s[16:17] offset:3072 nt
	s_add_u32 s16, s16, 0xfa0000
	s_addc_u32 s17, s17, 0
	v_cndmask_b32_e64 v30, 0, v30, s[18:19]
	v_cndmask_b32_e64 v31, 0, v31, s[18:19]
	v_cndmask_b32_e64 v32, 0, v32, s[18:19]
	v_cndmask_b32_e64 v33, 0, v33, s[18:19]
	v_max3_f32 v41, |v18|, |v19|, |v20|
	v_max3_f32 v42, |v21|, |v22|, |v23|
	v_max3_f32 v43, |v24|, |v25|, |v26|
	v_max3_f32 v44, |v27|, |v28|, |v29|
	v_max3_f32 v48, |v30|, |v31|, |v32|
	v_max3_f32 v41, v41, v42, |v33|
	v_max3_f32 v43, v43, v44, v48
	v_max_f32_e32 v41, v41, v43
	v_pk_add_f32 v[2:3], v[2:3], v[18:19]
	v_pk_add_f32 v[4:5], v[4:5], v[20:21]
	v_max_f32_dpp v41, v41, v41 quad_perm:[1,0,3,2] row_mask:0xf bank_mask:0xf
	v_pk_add_f32 v[6:7], v[6:7], v[22:23]
	v_pk_add_f32 v[8:9], v[8:9], v[24:25]
	v_max_f32_dpp v41, v41, v41 quad_perm:[2,3,0,1] row_mask:0xf bank_mask:0xf
	v_pk_add_f32 v[10:11], v[10:11], v[26:27]
	v_pk_add_f32 v[12:13], v[12:13], v[28:29]
	v_max_f32_dpp v41, v41, v41 row_half_mirror row_mask:0xf bank_mask:0xf
	v_pk_add_f32 v[14:15], v[14:15], v[30:31]
	v_pk_add_f32 v[16:17], v[16:17], v[32:33]
	v_max_f32_dpp v41, v41, v41 row_mirror row_mask:0xf bank_mask:0xf
	s_nop 1
	v_max_f32_dpp v41, v41, v41 row_bcast:15 row_mask:0xa bank_mask:0xf
	s_nop 1
	v_max_f32_dpp v41, v41, v41 row_bcast:31 row_mask:0xc bank_mask:0xf
	s_nop 1
	v_readlane_b32 s28, v41, 63
	s_nop 1
	v_div_scale_f32 v48, s[30:31], s28, s28, v47
	v_rcp_f32_e32 v49, v48
	s_nop 0
	v_fma_f32 v50, -v48, v49, 1.0
	v_fmac_f32_e32 v49, v50, v49
	v_mov_b32_e32 v50, s28
	v_div_scale_f32 v50, vcc, s32, v50, s32
	v_mul_f32_e32 v51, v50, v49
	v_fma_f32 v52, -v48, v51, v50
	v_fmac_f32_e32 v51, v52, v49
	v_fma_f32 v48, -v48, v51, v50
	v_div_fmas_f32 v48, v48, v49, v51
	v_div_fixup_f32 v48, v48, s28, v47
	v_cmp_gt_f32_e64 vcc, s28, 0
	v_writelane_b32 v40, s28, 8
	s_nop 0
	v_cndmask_b32_e32 v48, 0, v48, vcc
	v_fmaak_f32 v49, v18, v48, 0x4b400000
	v_fmaak_f32 v50, v19, v48, 0x4b400000
	v_fmaak_f32 v51, v20, v48, 0x4b400000
	v_fmaak_f32 v52, v21, v48, 0x4b400000
	v_perm_b32 v49, v50, v49, s33
	v_perm_b32 v51, v52, v51, s34
	v_or_b32_e32 v88, v49, v51
	v_fmaak_f32 v41, v22, v48, 0x4b400000
	v_fmaak_f32 v42, v23, v48, 0x4b400000
	v_fmaak_f32 v43, v24, v48, 0x4b400000
	v_fmaak_f32 v44, v25, v48, 0x4b400000
	v_perm_b32 v41, v42, v41, s33
	v_perm_b32 v43, v44, v43, s34
	v_or_b32_e32 v89, v41, v43
	v_fmaak_f32 v49, v26, v48, 0x4b400000
	v_fmaak_f32 v50, v27, v48, 0x4b400000
	v_fmaak_f32 v51, v28, v48, 0x4b400000
	v_fmaak_f32 v52, v29, v48, 0x4b400000
	v_perm_b32 v49, v50, v49, s33
	v_perm_b32 v51, v52, v51, s34
	v_or_b32_e32 v90, v49, v51
	v_fmaak_f32 v41, v30, v48, 0x4b400000
	v_fmaak_f32 v42, v31, v48, 0x4b400000
	v_fmaak_f32 v43, v32, v48, 0x4b400000
	v_fmaak_f32 v44, v33, v48, 0x4b400000
	v_perm_b32 v41, v42, v41, s33
	v_perm_b32 v43, v44, v43, s34
	v_or_b32_e32 v91, v41, v43
	s_waitcnt vmcnt(0)
	ds_read_b128 v[18:21], v38 offset:4096
	ds_read_b128 v[22:25], v38 offset:5120
	ds_read_b128 v[26:29], v38 offset:6144
	ds_read_b128 v[30:33], v38 offset:7168
	s_waitcnt lgkmcnt(0)
	s_mov_b32 m0, s35
	s_nop 0
	global_load_lds_dwordx4 v34, s[16:17] nt
	global_load_lds_dwordx4 v34, s[16:17] offset:1024 nt
	global_load_lds_dwordx4 v34, s[16:17] offset:2048 nt
	global_load_lds_dwordx4 v35, s[16:17] offset:3072 nt
	s_add_u32 s16, s16, 0xfa0000
	s_addc_u32 s17, s17, 0
	v_cndmask_b32_e64 v30, 0, v30, s[18:19]
	v_cndmask_b32_e64 v31, 0, v31, s[18:19]
	v_cndmask_b32_e64 v32, 0, v32, s[18:19]
	v_cndmask_b32_e64 v33, 0, v33, s[18:19]
	v_max3_f32 v41, |v18|, |v19|, |v20|
	v_max3_f32 v42, |v21|, |v22|, |v23|
	v_max3_f32 v43, |v24|, |v25|, |v26|
	v_max3_f32 v44, |v27|, |v28|, |v29|
	v_max3_f32 v48, |v30|, |v31|, |v32|
	v_max3_f32 v41, v41, v42, |v33|
	v_max3_f32 v43, v43, v44, v48
	v_max_f32_e32 v41, v41, v43
	v_pk_add_f32 v[2:3], v[2:3], v[18:19]
	v_pk_add_f32 v[4:5], v[4:5], v[20:21]
	v_max_f32_dpp v41, v41, v41 quad_perm:[1,0,3,2] row_mask:0xf bank_mask:0xf
	v_pk_add_f32 v[6:7], v[6:7], v[22:23]
	v_pk_add_f32 v[8:9], v[8:9], v[24:25]
	v_max_f32_dpp v41, v41, v41 quad_perm:[2,3,0,1] row_mask:0xf bank_mask:0xf
	v_pk_add_f32 v[10:11], v[10:11], v[26:27]
	v_pk_add_f32 v[12:13], v[12:13], v[28:29]
	v_max_f32_dpp v41, v41, v41 row_half_mirror row_mask:0xf bank_mask:0xf
	v_pk_add_f32 v[14:15], v[14:15], v[30:31]
	v_pk_add_f32 v[16:17], v[16:17], v[32:33]
	v_max_f32_dpp v41, v41, v41 row_mirror row_mask:0xf bank_mask:0xf
	s_nop 1
	v_max_f32_dpp v41, v41, v41 row_bcast:15 row_mask:0xa bank_mask:0xf
	s_nop 1
	v_max_f32_dpp v41, v41, v41 row_bcast:31 row_mask:0xc bank_mask:0xf
	s_nop 1
	v_readlane_b32 s28, v41, 63
	s_nop 1
	v_div_scale_f32 v48, s[30:31], s28, s28, v47
	v_rcp_f32_e32 v49, v48
	s_nop 0
	v_fma_f32 v50, -v48, v49, 1.0
	v_fmac_f32_e32 v49, v50, v49
	v_mov_b32_e32 v50, s28
	v_div_scale_f32 v50, vcc, s32, v50, s32
	v_mul_f32_e32 v51, v50, v49
	v_fma_f32 v52, -v48, v51, v50
	v_fmac_f32_e32 v51, v52, v49
	v_fma_f32 v48, -v48, v51, v50
	v_div_fmas_f32 v48, v48, v49, v51
	v_div_fixup_f32 v48, v48, s28, v47
	v_cmp_gt_f32_e64 vcc, s28, 0
	v_writelane_b32 v40, s28, 9
	s_nop 0
	v_cndmask_b32_e32 v48, 0, v48, vcc
	v_fmaak_f32 v49, v18, v48, 0x4b400000
	v_fmaak_f32 v50, v19, v48, 0x4b400000
	v_fmaak_f32 v51, v20, v48, 0x4b400000
	v_fmaak_f32 v52, v21, v48, 0x4b400000
	v_perm_b32 v49, v50, v49, s33
	v_perm_b32 v51, v52, v51, s34
	v_or_b32_e32 v92, v49, v51
	v_fmaak_f32 v41, v22, v48, 0x4b400000
	v_fmaak_f32 v42, v23, v48, 0x4b400000
	v_fmaak_f32 v43, v24, v48, 0x4b400000
	v_fmaak_f32 v44, v25, v48, 0x4b400000
	v_perm_b32 v41, v42, v41, s33
	v_perm_b32 v43, v44, v43, s34
	v_or_b32_e32 v93, v41, v43
	v_fmaak_f32 v49, v26, v48, 0x4b400000
	v_fmaak_f32 v50, v27, v48, 0x4b400000
	v_fmaak_f32 v51, v28, v48, 0x4b400000
	v_fmaak_f32 v52, v29, v48, 0x4b400000
	v_perm_b32 v49, v50, v49, s33
	v_perm_b32 v51, v52, v51, s34
	v_or_b32_e32 v94, v49, v51
	v_fmaak_f32 v41, v30, v48, 0x4b400000
	v_fmaak_f32 v42, v31, v48, 0x4b400000
	v_fmaak_f32 v43, v32, v48, 0x4b400000
	v_fmaak_f32 v44, v33, v48, 0x4b400000
	v_perm_b32 v41, v42, v41, s33
	v_perm_b32 v43, v44, v43, s34
	v_or_b32_e32 v95, v41, v43
	s_waitcnt vmcnt(0)
	ds_read_b128 v[18:21], v38 offset:0
	ds_read_b128 v[22:25], v38 offset:1024
	ds_read_b128 v[26:29], v38 offset:2048
	ds_read_b128 v[30:33], v38 offset:3072
	s_waitcnt lgkmcnt(0)
	s_mov_b32 m0, s36
	s_nop 0
	global_load_lds_dwordx4 v34, s[16:17] nt
	global_load_lds_dwordx4 v34, s[16:17] offset:1024 nt
	global_load_lds_dwordx4 v34, s[16:17] offset:2048 nt
	global_load_lds_dwordx4 v35, s[16:17] offset:3072 nt
	s_add_u32 s16, s16, 0xfa0000
	s_addc_u32 s17, s17, 0
	v_cndmask_b32_e64 v30, 0, v30, s[18:19]
	v_cndmask_b32_e64 v31, 0, v31, s[18:19]
	v_cndmask_b32_e64 v32, 0, v32, s[18:19]
	v_cndmask_b32_e64 v33, 0, v33, s[18:19]
	v_max3_f32 v41, |v18|, |v19|, |v20|
	v_max3_f32 v42, |v21|, |v22|, |v23|
	v_max3_f32 v43, |v24|, |v25|, |v26|
	v_max3_f32 v44, |v27|, |v28|, |v29|
	v_max3_f32 v48, |v30|, |v31|, |v32|
	v_max3_f32 v41, v41, v42, |v33|
	v_max3_f32 v43, v43, v44, v48
	v_max_f32_e32 v41, v41, v43
	v_pk_add_f32 v[2:3], v[2:3], v[18:19]
	v_pk_add_f32 v[4:5], v[4:5], v[20:21]
	v_max_f32_dpp v41, v41, v41 quad_perm:[1,0,3,2] row_mask:0xf bank_mask:0xf
	v_pk_add_f32 v[6:7], v[6:7], v[22:23]
	v_pk_add_f32 v[8:9], v[8:9], v[24:25]
	v_max_f32_dpp v41, v41, v41 quad_perm:[2,3,0,1] row_mask:0xf bank_mask:0xf
	v_pk_add_f32 v[10:11], v[10:11], v[26:27]
	v_pk_add_f32 v[12:13], v[12:13], v[28:29]
	v_max_f32_dpp v41, v41, v41 row_half_mirror row_mask:0xf bank_mask:0xf
	v_pk_add_f32 v[14:15], v[14:15], v[30:31]
	v_pk_add_f32 v[16:17], v[16:17], v[32:33]
	v_max_f32_dpp v41, v41, v41 row_mirror row_mask:0xf bank_mask:0xf
	s_nop 1
	v_max_f32_dpp v41, v41, v41 row_bcast:15 row_mask:0xa bank_mask:0xf
	s_nop 1
	v_max_f32_dpp v41, v41, v41 row_bcast:31 row_mask:0xc bank_mask:0xf
	s_nop 1
	v_readlane_b32 s28, v41, 63
	s_nop 1
	v_div_scale_f32 v48, s[30:31], s28, s28, v47
	v_rcp_f32_e32 v49, v48
	s_nop 0
	v_fma_f32 v50, -v48, v49, 1.0
	v_fmac_f32_e32 v49, v50, v49
	v_mov_b32_e32 v50, s28
	v_div_scale_f32 v50, vcc, s32, v50, s32
	v_mul_f32_e32 v51, v50, v49
	v_fma_f32 v52, -v48, v51, v50
	v_fmac_f32_e32 v51, v52, v49
	v_fma_f32 v48, -v48, v51, v50
	v_div_fmas_f32 v48, v48, v49, v51
	v_div_fixup_f32 v48, v48, s28, v47
	v_cmp_gt_f32_e64 vcc, s28, 0
	v_writelane_b32 v40, s28, 10
	s_nop 0
	v_cndmask_b32_e32 v48, 0, v48, vcc
	v_fmaak_f32 v49, v18, v48, 0x4b400000
	v_fmaak_f32 v50, v19, v48, 0x4b400000
	v_fmaak_f32 v51, v20, v48, 0x4b400000
	v_fmaak_f32 v52, v21, v48, 0x4b400000
	v_perm_b32 v49, v50, v49, s33
	v_perm_b32 v51, v52, v51, s34
	v_or_b32_e32 v96, v49, v51
	v_fmaak_f32 v41, v22, v48, 0x4b400000
	v_fmaak_f32 v42, v23, v48, 0x4b400000
	v_fmaak_f32 v43, v24, v48, 0x4b400000
	v_fmaak_f32 v44, v25, v48, 0x4b400000
	v_perm_b32 v41, v42, v41, s33
	v_perm_b32 v43, v44, v43, s34
	v_or_b32_e32 v97, v41, v43
	v_fmaak_f32 v49, v26, v48, 0x4b400000
	v_fmaak_f32 v50, v27, v48, 0x4b400000
	v_fmaak_f32 v51, v28, v48, 0x4b400000
	v_fmaak_f32 v52, v29, v48, 0x4b400000
	v_perm_b32 v49, v50, v49, s33
	v_perm_b32 v51, v52, v51, s34
	v_or_b32_e32 v98, v49, v51
	v_fmaak_f32 v41, v30, v48, 0x4b400000
	v_fmaak_f32 v42, v31, v48, 0x4b400000
	v_fmaak_f32 v43, v32, v48, 0x4b400000
	v_fmaak_f32 v44, v33, v48, 0x4b400000
	v_perm_b32 v41, v42, v41, s33
	v_perm_b32 v43, v44, v43, s34
	v_or_b32_e32 v99, v41, v43
	s_waitcnt vmcnt(0)
	ds_read_b128 v[18:21], v38 offset:4096
	ds_read_b128 v[22:25], v38 offset:5120
	ds_read_b128 v[26:29], v38 offset:6144
	ds_read_b128 v[30:33], v38 offset:7168
	s_waitcnt lgkmcnt(0)
	s_mov_b32 m0, s35
	s_nop 0
	global_load_lds_dwordx4 v34, s[16:17] nt
	global_load_lds_dwordx4 v34, s[16:17] offset:1024 nt
	global_load_lds_dwordx4 v34, s[16:17] offset:2048 nt
	global_load_lds_dwordx4 v35, s[16:17] offset:3072 nt
	s_add_u32 s16, s16, 0xfa0000
	s_addc_u32 s17, s17, 0
	v_cndmask_b32_e64 v30, 0, v30, s[18:19]
	v_cndmask_b32_e64 v31, 0, v31, s[18:19]
	v_cndmask_b32_e64 v32, 0, v32, s[18:19]
	v_cndmask_b32_e64 v33, 0, v33, s[18:19]
	v_max3_f32 v41, |v18|, |v19|, |v20|
	v_max3_f32 v42, |v21|, |v22|, |v23|
	v_max3_f32 v43, |v24|, |v25|, |v26|
	v_max3_f32 v44, |v27|, |v28|, |v29|
	v_max3_f32 v48, |v30|, |v31|, |v32|
	v_max3_f32 v41, v41, v42, |v33|
	v_max3_f32 v43, v43, v44, v48
	v_max_f32_e32 v41, v41, v43
	v_pk_add_f32 v[2:3], v[2:3], v[18:19]
	v_pk_add_f32 v[4:5], v[4:5], v[20:21]
	v_max_f32_dpp v41, v41, v41 quad_perm:[1,0,3,2] row_mask:0xf bank_mask:0xf
	v_pk_add_f32 v[6:7], v[6:7], v[22:23]
	v_pk_add_f32 v[8:9], v[8:9], v[24:25]
	v_max_f32_dpp v41, v41, v41 quad_perm:[2,3,0,1] row_mask:0xf bank_mask:0xf
	v_pk_add_f32 v[10:11], v[10:11], v[26:27]
	v_pk_add_f32 v[12:13], v[12:13], v[28:29]
	v_max_f32_dpp v41, v41, v41 row_half_mirror row_mask:0xf bank_mask:0xf
	v_pk_add_f32 v[14:15], v[14:15], v[30:31]
	v_pk_add_f32 v[16:17], v[16:17], v[32:33]
	v_max_f32_dpp v41, v41, v41 row_mirror row_mask:0xf bank_mask:0xf
	s_nop 1
	v_max_f32_dpp v41, v41, v41 row_bcast:15 row_mask:0xa bank_mask:0xf
	s_nop 1
	v_max_f32_dpp v41, v41, v41 row_bcast:31 row_mask:0xc bank_mask:0xf
	s_nop 1
	v_readlane_b32 s28, v41, 63
	s_nop 1
	v_div_scale_f32 v48, s[30:31], s28, s28, v47
	v_rcp_f32_e32 v49, v48
	s_nop 0
	v_fma_f32 v50, -v48, v49, 1.0
	v_fmac_f32_e32 v49, v50, v49
	v_mov_b32_e32 v50, s28
	v_div_scale_f32 v50, vcc, s32, v50, s32
	v_mul_f32_e32 v51, v50, v49
	v_fma_f32 v52, -v48, v51, v50
	v_fmac_f32_e32 v51, v52, v49
	v_fma_f32 v48, -v48, v51, v50
	v_div_fmas_f32 v48, v48, v49, v51
	v_div_fixup_f32 v48, v48, s28, v47
	v_cmp_gt_f32_e64 vcc, s28, 0
	v_writelane_b32 v40, s28, 11
	s_nop 0
	v_cndmask_b32_e32 v48, 0, v48, vcc
	v_fmaak_f32 v49, v18, v48, 0x4b400000
	v_fmaak_f32 v50, v19, v48, 0x4b400000
	v_fmaak_f32 v51, v20, v48, 0x4b400000
	v_fmaak_f32 v52, v21, v48, 0x4b400000
	v_perm_b32 v49, v50, v49, s33
	v_perm_b32 v51, v52, v51, s34
	v_or_b32_e32 v100, v49, v51
	v_fmaak_f32 v41, v22, v48, 0x4b400000
	v_fmaak_f32 v42, v23, v48, 0x4b400000
	v_fmaak_f32 v43, v24, v48, 0x4b400000
	v_fmaak_f32 v44, v25, v48, 0x4b400000
	v_perm_b32 v41, v42, v41, s33
	v_perm_b32 v43, v44, v43, s34
	v_or_b32_e32 v101, v41, v43
	v_fmaak_f32 v49, v26, v48, 0x4b400000
	v_fmaak_f32 v50, v27, v48, 0x4b400000
	v_fmaak_f32 v51, v28, v48, 0x4b400000
	v_fmaak_f32 v52, v29, v48, 0x4b400000
	v_perm_b32 v49, v50, v49, s33
	v_perm_b32 v51, v52, v51, s34
	v_or_b32_e32 v102, v49, v51
	v_fmaak_f32 v41, v30, v48, 0x4b400000
	v_fmaak_f32 v42, v31, v48, 0x4b400000
	v_fmaak_f32 v43, v32, v48, 0x4b400000
	v_fmaak_f32 v44, v33, v48, 0x4b400000
	v_perm_b32 v41, v42, v41, s33
	v_perm_b32 v43, v44, v43, s34
	v_or_b32_e32 v103, v41, v43
	s_waitcnt vmcnt(0)
	ds_read_b128 v[18:21], v38 offset:0
	ds_read_b128 v[22:25], v38 offset:1024
	ds_read_b128 v[26:29], v38 offset:2048
	ds_read_b128 v[30:33], v38 offset:3072
	s_waitcnt lgkmcnt(0)
	s_mov_b32 m0, s36
	s_nop 0
	global_load_lds_dwordx4 v34, s[16:17] nt
	global_load_lds_dwordx4 v34, s[16:17] offset:1024 nt
	global_load_lds_dwordx4 v34, s[16:17] offset:2048 nt
	global_load_lds_dwordx4 v35, s[16:17] offset:3072 nt
	s_add_u32 s16, s16, 0xfa0000
	s_addc_u32 s17, s17, 0
	v_cndmask_b32_e64 v30, 0, v30, s[18:19]
	v_cndmask_b32_e64 v31, 0, v31, s[18:19]
	v_cndmask_b32_e64 v32, 0, v32, s[18:19]
	v_cndmask_b32_e64 v33, 0, v33, s[18:19]
	v_max3_f32 v41, |v18|, |v19|, |v20|
	v_max3_f32 v42, |v21|, |v22|, |v23|
	v_max3_f32 v43, |v24|, |v25|, |v26|
	v_max3_f32 v44, |v27|, |v28|, |v29|
	v_max3_f32 v48, |v30|, |v31|, |v32|
	v_max3_f32 v41, v41, v42, |v33|
	v_max3_f32 v43, v43, v44, v48
	v_max_f32_e32 v41, v41, v43
	v_pk_add_f32 v[2:3], v[2:3], v[18:19]
	v_pk_add_f32 v[4:5], v[4:5], v[20:21]
	v_max_f32_dpp v41, v41, v41 quad_perm:[1,0,3,2] row_mask:0xf bank_mask:0xf
	v_pk_add_f32 v[6:7], v[6:7], v[22:23]
	v_pk_add_f32 v[8:9], v[8:9], v[24:25]
	v_max_f32_dpp v41, v41, v41 quad_perm:[2,3,0,1] row_mask:0xf bank_mask:0xf
	v_pk_add_f32 v[10:11], v[10:11], v[26:27]
	v_pk_add_f32 v[12:13], v[12:13], v[28:29]
	v_max_f32_dpp v41, v41, v41 row_half_mirror row_mask:0xf bank_mask:0xf
	v_pk_add_f32 v[14:15], v[14:15], v[30:31]
	v_pk_add_f32 v[16:17], v[16:17], v[32:33]
	v_max_f32_dpp v41, v41, v41 row_mirror row_mask:0xf bank_mask:0xf
	s_nop 1
	v_max_f32_dpp v41, v41, v41 row_bcast:15 row_mask:0xa bank_mask:0xf
	s_nop 1
	v_max_f32_dpp v41, v41, v41 row_bcast:31 row_mask:0xc bank_mask:0xf
	s_nop 1
	v_readlane_b32 s28, v41, 63
	s_nop 1
	v_div_scale_f32 v48, s[30:31], s28, s28, v47
	v_rcp_f32_e32 v49, v48
	s_nop 0
	v_fma_f32 v50, -v48, v49, 1.0
	v_fmac_f32_e32 v49, v50, v49
	v_mov_b32_e32 v50, s28
	v_div_scale_f32 v50, vcc, s32, v50, s32
	v_mul_f32_e32 v51, v50, v49
	v_fma_f32 v52, -v48, v51, v50
	v_fmac_f32_e32 v51, v52, v49
	v_fma_f32 v48, -v48, v51, v50
	v_div_fmas_f32 v48, v48, v49, v51
	v_div_fixup_f32 v48, v48, s28, v47
	v_cmp_gt_f32_e64 vcc, s28, 0
	v_writelane_b32 v40, s28, 12
	s_nop 0
	v_cndmask_b32_e32 v48, 0, v48, vcc
	v_fmaak_f32 v49, v18, v48, 0x4b400000
	v_fmaak_f32 v50, v19, v48, 0x4b400000
	v_fmaak_f32 v51, v20, v48, 0x4b400000
	v_fmaak_f32 v52, v21, v48, 0x4b400000
	v_perm_b32 v49, v50, v49, s33
	v_perm_b32 v51, v52, v51, s34
	v_or_b32_e32 v104, v49, v51
	v_fmaak_f32 v41, v22, v48, 0x4b400000
	v_fmaak_f32 v42, v23, v48, 0x4b400000
	v_fmaak_f32 v43, v24, v48, 0x4b400000
	v_fmaak_f32 v44, v25, v48, 0x4b400000
	v_perm_b32 v41, v42, v41, s33
	v_perm_b32 v43, v44, v43, s34
	v_or_b32_e32 v105, v41, v43
	v_fmaak_f32 v49, v26, v48, 0x4b400000
	v_fmaak_f32 v50, v27, v48, 0x4b400000
	v_fmaak_f32 v51, v28, v48, 0x4b400000
	v_fmaak_f32 v52, v29, v48, 0x4b400000
	v_perm_b32 v49, v50, v49, s33
	v_perm_b32 v51, v52, v51, s34
	v_or_b32_e32 v106, v49, v51
	v_fmaak_f32 v41, v30, v48, 0x4b400000
	v_fmaak_f32 v42, v31, v48, 0x4b400000
	v_fmaak_f32 v43, v32, v48, 0x4b400000
	v_fmaak_f32 v44, v33, v48, 0x4b400000
	v_perm_b32 v41, v42, v41, s33
	v_perm_b32 v43, v44, v43, s34
	v_or_b32_e32 v107, v41, v43
	s_waitcnt vmcnt(0)
	ds_read_b128 v[18:21], v38 offset:4096
	ds_read_b128 v[22:25], v38 offset:5120
	ds_read_b128 v[26:29], v38 offset:6144
	ds_read_b128 v[30:33], v38 offset:7168
	s_waitcnt lgkmcnt(0)
	s_mov_b32 m0, s35
	s_nop 0
	global_load_lds_dwordx4 v34, s[16:17] nt
	global_load_lds_dwordx4 v34, s[16:17] offset:1024 nt
	global_load_lds_dwordx4 v34, s[16:17] offset:2048 nt
	global_load_lds_dwordx4 v35, s[16:17] offset:3072 nt
	s_add_u32 s16, s16, 0xfa0000
	s_addc_u32 s17, s17, 0
	v_cndmask_b32_e64 v30, 0, v30, s[18:19]
	v_cndmask_b32_e64 v31, 0, v31, s[18:19]
	v_cndmask_b32_e64 v32, 0, v32, s[18:19]
	v_cndmask_b32_e64 v33, 0, v33, s[18:19]
	v_max3_f32 v41, |v18|, |v19|, |v20|
	v_max3_f32 v42, |v21|, |v22|, |v23|
	v_max3_f32 v43, |v24|, |v25|, |v26|
	v_max3_f32 v44, |v27|, |v28|, |v29|
	v_max3_f32 v48, |v30|, |v31|, |v32|
	v_max3_f32 v41, v41, v42, |v33|
	v_max3_f32 v43, v43, v44, v48
	v_max_f32_e32 v41, v41, v43
	v_pk_add_f32 v[2:3], v[2:3], v[18:19]
	v_pk_add_f32 v[4:5], v[4:5], v[20:21]
	v_max_f32_dpp v41, v41, v41 quad_perm:[1,0,3,2] row_mask:0xf bank_mask:0xf
	v_pk_add_f32 v[6:7], v[6:7], v[22:23]
	v_pk_add_f32 v[8:9], v[8:9], v[24:25]
	v_max_f32_dpp v41, v41, v41 quad_perm:[2,3,0,1] row_mask:0xf bank_mask:0xf
	v_pk_add_f32 v[10:11], v[10:11], v[26:27]
	v_pk_add_f32 v[12:13], v[12:13], v[28:29]
	v_max_f32_dpp v41, v41, v41 row_half_mirror row_mask:0xf bank_mask:0xf
	v_pk_add_f32 v[14:15], v[14:15], v[30:31]
	v_pk_add_f32 v[16:17], v[16:17], v[32:33]
	v_max_f32_dpp v41, v41, v41 row_mirror row_mask:0xf bank_mask:0xf
	s_nop 1
	v_max_f32_dpp v41, v41, v41 row_bcast:15 row_mask:0xa bank_mask:0xf
	s_nop 1
	v_max_f32_dpp v41, v41, v41 row_bcast:31 row_mask:0xc bank_mask:0xf
	s_nop 1
	v_readlane_b32 s28, v41, 63
	s_nop 1
	v_div_scale_f32 v48, s[30:31], s28, s28, v47
	v_rcp_f32_e32 v49, v48
	s_nop 0
	v_fma_f32 v50, -v48, v49, 1.0
	v_fmac_f32_e32 v49, v50, v49
	v_mov_b32_e32 v50, s28
	v_div_scale_f32 v50, vcc, s32, v50, s32
	v_mul_f32_e32 v51, v50, v49
	v_fma_f32 v52, -v48, v51, v50
	v_fmac_f32_e32 v51, v52, v49
	v_fma_f32 v48, -v48, v51, v50
	v_div_fmas_f32 v48, v48, v49, v51
	v_div_fixup_f32 v48, v48, s28, v47
	v_cmp_gt_f32_e64 vcc, s28, 0
	v_writelane_b32 v40, s28, 13
	s_nop 0
	v_cndmask_b32_e32 v48, 0, v48, vcc
	v_fmaak_f32 v49, v18, v48, 0x4b400000
	v_fmaak_f32 v50, v19, v48, 0x4b400000
	v_fmaak_f32 v51, v20, v48, 0x4b400000
	v_fmaak_f32 v52, v21, v48, 0x4b400000
	v_perm_b32 v49, v50, v49, s33
	v_perm_b32 v51, v52, v51, s34
	v_or_b32_e32 v108, v49, v51
	v_fmaak_f32 v41, v22, v48, 0x4b400000
	v_fmaak_f32 v42, v23, v48, 0x4b400000
	v_fmaak_f32 v43, v24, v48, 0x4b400000
	v_fmaak_f32 v44, v25, v48, 0x4b400000
	v_perm_b32 v41, v42, v41, s33
	v_perm_b32 v43, v44, v43, s34
	v_or_b32_e32 v109, v41, v43
	v_fmaak_f32 v49, v26, v48, 0x4b400000
	v_fmaak_f32 v50, v27, v48, 0x4b400000
	v_fmaak_f32 v51, v28, v48, 0x4b400000
	v_fmaak_f32 v52, v29, v48, 0x4b400000
	v_perm_b32 v49, v50, v49, s33
	v_perm_b32 v51, v52, v51, s34
	v_or_b32_e32 v110, v49, v51
	v_fmaak_f32 v41, v30, v48, 0x4b400000
	v_fmaak_f32 v42, v31, v48, 0x4b400000
	v_fmaak_f32 v43, v32, v48, 0x4b400000
	v_fmaak_f32 v44, v33, v48, 0x4b400000
	v_perm_b32 v41, v42, v41, s33
	v_perm_b32 v43, v44, v43, s34
	v_or_b32_e32 v111, v41, v43
	s_waitcnt vmcnt(0)
	ds_read_b128 v[18:21], v38 offset:0
	ds_read_b128 v[22:25], v38 offset:1024
	ds_read_b128 v[26:29], v38 offset:2048
	ds_read_b128 v[30:33], v38 offset:3072
	s_waitcnt lgkmcnt(0)
	s_mov_b32 m0, s36
	s_nop 0
	global_load_lds_dwordx4 v34, s[16:17] nt
	global_load_lds_dwordx4 v34, s[16:17] offset:1024 nt
	global_load_lds_dwordx4 v34, s[16:17] offset:2048 nt
	global_load_lds_dwordx4 v35, s[16:17] offset:3072 nt
	s_add_u32 s16, s16, 0xfa0000
	s_addc_u32 s17, s17, 0
	v_cndmask_b32_e64 v30, 0, v30, s[18:19]
	v_cndmask_b32_e64 v31, 0, v31, s[18:19]
	v_cndmask_b32_e64 v32, 0, v32, s[18:19]
	v_cndmask_b32_e64 v33, 0, v33, s[18:19]
	v_max3_f32 v41, |v18|, |v19|, |v20|
	v_max3_f32 v42, |v21|, |v22|, |v23|
	v_max3_f32 v43, |v24|, |v25|, |v26|
	v_max3_f32 v44, |v27|, |v28|, |v29|
	v_max3_f32 v48, |v30|, |v31|, |v32|
	v_max3_f32 v41, v41, v42, |v33|
	v_max3_f32 v43, v43, v44, v48
	v_max_f32_e32 v41, v41, v43
	v_pk_add_f32 v[2:3], v[2:3], v[18:19]
	v_pk_add_f32 v[4:5], v[4:5], v[20:21]
	v_max_f32_dpp v41, v41, v41 quad_perm:[1,0,3,2] row_mask:0xf bank_mask:0xf
	v_pk_add_f32 v[6:7], v[6:7], v[22:23]
	v_pk_add_f32 v[8:9], v[8:9], v[24:25]
	v_max_f32_dpp v41, v41, v41 quad_perm:[2,3,0,1] row_mask:0xf bank_mask:0xf
	v_pk_add_f32 v[10:11], v[10:11], v[26:27]
	v_pk_add_f32 v[12:13], v[12:13], v[28:29]
	v_max_f32_dpp v41, v41, v41 row_half_mirror row_mask:0xf bank_mask:0xf
	v_pk_add_f32 v[14:15], v[14:15], v[30:31]
	v_pk_add_f32 v[16:17], v[16:17], v[32:33]
	v_max_f32_dpp v41, v41, v41 row_mirror row_mask:0xf bank_mask:0xf
	s_nop 1
	v_max_f32_dpp v41, v41, v41 row_bcast:15 row_mask:0xa bank_mask:0xf
	s_nop 1
	v_max_f32_dpp v41, v41, v41 row_bcast:31 row_mask:0xc bank_mask:0xf
	s_nop 1
	v_readlane_b32 s28, v41, 63
	s_nop 1
	v_div_scale_f32 v48, s[30:31], s28, s28, v47
	v_rcp_f32_e32 v49, v48
	s_nop 0
	v_fma_f32 v50, -v48, v49, 1.0
	v_fmac_f32_e32 v49, v50, v49
	v_mov_b32_e32 v50, s28
	v_div_scale_f32 v50, vcc, s32, v50, s32
	v_mul_f32_e32 v51, v50, v49
	v_fma_f32 v52, -v48, v51, v50
	v_fmac_f32_e32 v51, v52, v49
	v_fma_f32 v48, -v48, v51, v50
	v_div_fmas_f32 v48, v48, v49, v51
	v_div_fixup_f32 v48, v48, s28, v47
	v_cmp_gt_f32_e64 vcc, s28, 0
	v_writelane_b32 v40, s28, 14
	s_nop 0
	v_cndmask_b32_e32 v48, 0, v48, vcc
	v_fmaak_f32 v49, v18, v48, 0x4b400000
	v_fmaak_f32 v50, v19, v48, 0x4b400000
	v_fmaak_f32 v51, v20, v48, 0x4b400000
	v_fmaak_f32 v52, v21, v48, 0x4b400000
	v_perm_b32 v49, v50, v49, s33
	v_perm_b32 v51, v52, v51, s34
	v_or_b32_e32 v112, v49, v51
	v_fmaak_f32 v41, v22, v48, 0x4b400000
	v_fmaak_f32 v42, v23, v48, 0x4b400000
	v_fmaak_f32 v43, v24, v48, 0x4b400000
	v_fmaak_f32 v44, v25, v48, 0x4b400000
	v_perm_b32 v41, v42, v41, s33
	v_perm_b32 v43, v44, v43, s34
	v_or_b32_e32 v113, v41, v43
	v_fmaak_f32 v49, v26, v48, 0x4b400000
	v_fmaak_f32 v50, v27, v48, 0x4b400000
	v_fmaak_f32 v51, v28, v48, 0x4b400000
	v_fmaak_f32 v52, v29, v48, 0x4b400000
	v_perm_b32 v49, v50, v49, s33
	v_perm_b32 v51, v52, v51, s34
	v_or_b32_e32 v114, v49, v51
	v_fmaak_f32 v41, v30, v48, 0x4b400000
	v_fmaak_f32 v42, v31, v48, 0x4b400000
	v_fmaak_f32 v43, v32, v48, 0x4b400000
	v_fmaak_f32 v44, v33, v48, 0x4b400000
	v_perm_b32 v41, v42, v41, s33
	v_perm_b32 v43, v44, v43, s34
	v_or_b32_e32 v115, v41, v43
	s_waitcnt vmcnt(0)
	ds_read_b128 v[18:21], v38 offset:4096
	ds_read_b128 v[22:25], v38 offset:5120
	ds_read_b128 v[26:29], v38 offset:6144
	ds_read_b128 v[30:33], v38 offset:7168
	s_waitcnt lgkmcnt(0)
	s_mov_b32 m0, s35
	s_nop 0
	global_load_lds_dwordx4 v34, s[16:17] nt
	global_load_lds_dwordx4 v34, s[16:17] offset:1024 nt
	global_load_lds_dwordx4 v34, s[16:17] offset:2048 nt
	global_load_lds_dwordx4 v35, s[16:17] offset:3072 nt
	s_add_u32 s16, s16, 0xfa0000
	s_addc_u32 s17, s17, 0
	v_cndmask_b32_e64 v30, 0, v30, s[18:19]
	v_cndmask_b32_e64 v31, 0, v31, s[18:19]
	v_cndmask_b32_e64 v32, 0, v32, s[18:19]
	v_cndmask_b32_e64 v33, 0, v33, s[18:19]
	v_max3_f32 v41, |v18|, |v19|, |v20|
	v_max3_f32 v42, |v21|, |v22|, |v23|
	v_max3_f32 v43, |v24|, |v25|, |v26|
	v_max3_f32 v44, |v27|, |v28|, |v29|
	v_max3_f32 v48, |v30|, |v31|, |v32|
	v_max3_f32 v41, v41, v42, |v33|
	v_max3_f32 v43, v43, v44, v48
	v_max_f32_e32 v41, v41, v43
	v_pk_add_f32 v[2:3], v[2:3], v[18:19]
	v_pk_add_f32 v[4:5], v[4:5], v[20:21]
	v_max_f32_dpp v41, v41, v41 quad_perm:[1,0,3,2] row_mask:0xf bank_mask:0xf
	v_pk_add_f32 v[6:7], v[6:7], v[22:23]
	v_pk_add_f32 v[8:9], v[8:9], v[24:25]
	v_max_f32_dpp v41, v41, v41 quad_perm:[2,3,0,1] row_mask:0xf bank_mask:0xf
	v_pk_add_f32 v[10:11], v[10:11], v[26:27]
	v_pk_add_f32 v[12:13], v[12:13], v[28:29]
	v_max_f32_dpp v41, v41, v41 row_half_mirror row_mask:0xf bank_mask:0xf
	v_pk_add_f32 v[14:15], v[14:15], v[30:31]
	v_pk_add_f32 v[16:17], v[16:17], v[32:33]
	v_max_f32_dpp v41, v41, v41 row_mirror row_mask:0xf bank_mask:0xf
	s_nop 1
	v_max_f32_dpp v41, v41, v41 row_bcast:15 row_mask:0xa bank_mask:0xf
	s_nop 1
	v_max_f32_dpp v41, v41, v41 row_bcast:31 row_mask:0xc bank_mask:0xf
	s_nop 1
	v_readlane_b32 s28, v41, 63
	s_nop 1
	v_div_scale_f32 v48, s[30:31], s28, s28, v47
	v_rcp_f32_e32 v49, v48
	s_nop 0
	v_fma_f32 v50, -v48, v49, 1.0
	v_fmac_f32_e32 v49, v50, v49
	v_mov_b32_e32 v50, s28
	v_div_scale_f32 v50, vcc, s32, v50, s32
	v_mul_f32_e32 v51, v50, v49
	v_fma_f32 v52, -v48, v51, v50
	v_fmac_f32_e32 v51, v52, v49
	v_fma_f32 v48, -v48, v51, v50
	v_div_fmas_f32 v48, v48, v49, v51
	v_div_fixup_f32 v48, v48, s28, v47
	v_cmp_gt_f32_e64 vcc, s28, 0
	v_writelane_b32 v40, s28, 15
	s_nop 0
	v_cndmask_b32_e32 v48, 0, v48, vcc
	v_fmaak_f32 v49, v18, v48, 0x4b400000
	v_fmaak_f32 v50, v19, v48, 0x4b400000
	v_fmaak_f32 v51, v20, v48, 0x4b400000
	v_fmaak_f32 v52, v21, v48, 0x4b400000
	v_perm_b32 v49, v50, v49, s33
	v_perm_b32 v51, v52, v51, s34
	v_or_b32_e32 v116, v49, v51
	v_fmaak_f32 v41, v22, v48, 0x4b400000
	v_fmaak_f32 v42, v23, v48, 0x4b400000
	v_fmaak_f32 v43, v24, v48, 0x4b400000
	v_fmaak_f32 v44, v25, v48, 0x4b400000
	v_perm_b32 v41, v42, v41, s33
	v_perm_b32 v43, v44, v43, s34
	v_or_b32_e32 v117, v41, v43
	v_fmaak_f32 v49, v26, v48, 0x4b400000
	v_fmaak_f32 v50, v27, v48, 0x4b400000
	v_fmaak_f32 v51, v28, v48, 0x4b400000
	v_fmaak_f32 v52, v29, v48, 0x4b400000
	v_perm_b32 v49, v50, v49, s33
	v_perm_b32 v51, v52, v51, s34
	v_or_b32_e32 v118, v49, v51
	v_fmaak_f32 v41, v30, v48, 0x4b400000
	v_fmaak_f32 v42, v31, v48, 0x4b400000
	v_fmaak_f32 v43, v32, v48, 0x4b400000
	v_fmaak_f32 v44, v33, v48, 0x4b400000
	v_perm_b32 v41, v42, v41, s33
	v_perm_b32 v43, v44, v43, s34
	v_or_b32_e32 v119, v41, v43
	s_waitcnt vmcnt(0)
	ds_read_b128 v[18:21], v38 offset:0
	ds_read_b128 v[22:25], v38 offset:1024
	ds_read_b128 v[26:29], v38 offset:2048
	ds_read_b128 v[30:33], v38 offset:3072
	s_waitcnt lgkmcnt(0)
	s_mov_b32 m0, s36
	s_nop 0
	global_load_lds_dwordx4 v34, s[16:17] nt
	global_load_lds_dwordx4 v34, s[16:17] offset:1024 nt
	global_load_lds_dwordx4 v34, s[16:17] offset:2048 nt
	global_load_lds_dwordx4 v35, s[16:17] offset:3072 nt
	s_add_u32 s16, s16, 0xfa0000
	s_addc_u32 s17, s17, 0
	v_cndmask_b32_e64 v30, 0, v30, s[18:19]
	v_cndmask_b32_e64 v31, 0, v31, s[18:19]
	v_cndmask_b32_e64 v32, 0, v32, s[18:19]
	v_cndmask_b32_e64 v33, 0, v33, s[18:19]
	v_max3_f32 v41, |v18|, |v19|, |v20|
	v_max3_f32 v42, |v21|, |v22|, |v23|
	v_max3_f32 v43, |v24|, |v25|, |v26|
	v_max3_f32 v44, |v27|, |v28|, |v29|
	v_max3_f32 v48, |v30|, |v31|, |v32|
	v_max3_f32 v41, v41, v42, |v33|
	v_max3_f32 v43, v43, v44, v48
	v_max_f32_e32 v41, v41, v43
	v_pk_add_f32 v[2:3], v[2:3], v[18:19]
	v_pk_add_f32 v[4:5], v[4:5], v[20:21]
	v_max_f32_dpp v41, v41, v41 quad_perm:[1,0,3,2] row_mask:0xf bank_mask:0xf
	v_pk_add_f32 v[6:7], v[6:7], v[22:23]
	v_pk_add_f32 v[8:9], v[8:9], v[24:25]
	v_max_f32_dpp v41, v41, v41 quad_perm:[2,3,0,1] row_mask:0xf bank_mask:0xf
	v_pk_add_f32 v[10:11], v[10:11], v[26:27]
	v_pk_add_f32 v[12:13], v[12:13], v[28:29]
	v_max_f32_dpp v41, v41, v41 row_half_mirror row_mask:0xf bank_mask:0xf
	v_pk_add_f32 v[14:15], v[14:15], v[30:31]
	v_pk_add_f32 v[16:17], v[16:17], v[32:33]
	v_max_f32_dpp v41, v41, v41 row_mirror row_mask:0xf bank_mask:0xf
	s_nop 1
	v_max_f32_dpp v41, v41, v41 row_bcast:15 row_mask:0xa bank_mask:0xf
	s_nop 1
	v_max_f32_dpp v41, v41, v41 row_bcast:31 row_mask:0xc bank_mask:0xf
	s_nop 1
	v_readlane_b32 s28, v41, 63
	s_nop 1
	v_div_scale_f32 v48, s[30:31], s28, s28, v47
	v_rcp_f32_e32 v49, v48
	s_nop 0
	v_fma_f32 v50, -v48, v49, 1.0
	v_fmac_f32_e32 v49, v50, v49
	v_mov_b32_e32 v50, s28
	v_div_scale_f32 v50, vcc, s32, v50, s32
	v_mul_f32_e32 v51, v50, v49
	v_fma_f32 v52, -v48, v51, v50
	v_fmac_f32_e32 v51, v52, v49
	v_fma_f32 v48, -v48, v51, v50
	v_div_fmas_f32 v48, v48, v49, v51
	v_div_fixup_f32 v48, v48, s28, v47
	v_cmp_gt_f32_e64 vcc, s28, 0
	v_writelane_b32 v40, s28, 16
	s_nop 0
	v_cndmask_b32_e32 v48, 0, v48, vcc
	v_fmaak_f32 v49, v18, v48, 0x4b400000
	v_fmaak_f32 v50, v19, v48, 0x4b400000
	v_fmaak_f32 v51, v20, v48, 0x4b400000
	v_fmaak_f32 v52, v21, v48, 0x4b400000
	v_perm_b32 v49, v50, v49, s33
	v_perm_b32 v51, v52, v51, s34
	v_or_b32_e32 v120, v49, v51
	v_fmaak_f32 v41, v22, v48, 0x4b400000
	v_fmaak_f32 v42, v23, v48, 0x4b400000
	v_fmaak_f32 v43, v24, v48, 0x4b400000
	v_fmaak_f32 v44, v25, v48, 0x4b400000
	v_perm_b32 v41, v42, v41, s33
	v_perm_b32 v43, v44, v43, s34
	v_or_b32_e32 v121, v41, v43
	v_fmaak_f32 v49, v26, v48, 0x4b400000
	v_fmaak_f32 v50, v27, v48, 0x4b400000
	v_fmaak_f32 v51, v28, v48, 0x4b400000
	v_fmaak_f32 v52, v29, v48, 0x4b400000
	v_perm_b32 v49, v50, v49, s33
	v_perm_b32 v51, v52, v51, s34
	v_or_b32_e32 v122, v49, v51
	v_fmaak_f32 v41, v30, v48, 0x4b400000
	v_fmaak_f32 v42, v31, v48, 0x4b400000
	v_fmaak_f32 v43, v32, v48, 0x4b400000
	v_fmaak_f32 v44, v33, v48, 0x4b400000
	v_perm_b32 v41, v42, v41, s33
	v_perm_b32 v43, v44, v43, s34
	v_or_b32_e32 v123, v41, v43
	s_waitcnt vmcnt(0)
	ds_read_b128 v[18:21], v38 offset:4096
	ds_read_b128 v[22:25], v38 offset:5120
	ds_read_b128 v[26:29], v38 offset:6144
	ds_read_b128 v[30:33], v38 offset:7168
	s_waitcnt lgkmcnt(0)
	s_mov_b32 m0, s35
	s_nop 0
	global_load_lds_dwordx4 v34, s[16:17] nt
	global_load_lds_dwordx4 v34, s[16:17] offset:1024 nt
	global_load_lds_dwordx4 v34, s[16:17] offset:2048 nt
	global_load_lds_dwordx4 v35, s[16:17] offset:3072 nt
	s_add_u32 s16, s16, 0xfa0000
	s_addc_u32 s17, s17, 0
	v_cndmask_b32_e64 v30, 0, v30, s[18:19]
	v_cndmask_b32_e64 v31, 0, v31, s[18:19]
	v_cndmask_b32_e64 v32, 0, v32, s[18:19]
	v_cndmask_b32_e64 v33, 0, v33, s[18:19]
	v_max3_f32 v41, |v18|, |v19|, |v20|
	v_max3_f32 v42, |v21|, |v22|, |v23|
	v_max3_f32 v43, |v24|, |v25|, |v26|
	v_max3_f32 v44, |v27|, |v28|, |v29|
	v_max3_f32 v48, |v30|, |v31|, |v32|
	v_max3_f32 v41, v41, v42, |v33|
	v_max3_f32 v43, v43, v44, v48
	v_max_f32_e32 v41, v41, v43
	v_pk_add_f32 v[2:3], v[2:3], v[18:19]
	v_pk_add_f32 v[4:5], v[4:5], v[20:21]
	v_max_f32_dpp v41, v41, v41 quad_perm:[1,0,3,2] row_mask:0xf bank_mask:0xf
	v_pk_add_f32 v[6:7], v[6:7], v[22:23]
	v_pk_add_f32 v[8:9], v[8:9], v[24:25]
	v_max_f32_dpp v41, v41, v41 quad_perm:[2,3,0,1] row_mask:0xf bank_mask:0xf
	v_pk_add_f32 v[10:11], v[10:11], v[26:27]
	v_pk_add_f32 v[12:13], v[12:13], v[28:29]
	v_max_f32_dpp v41, v41, v41 row_half_mirror row_mask:0xf bank_mask:0xf
	v_pk_add_f32 v[14:15], v[14:15], v[30:31]
	v_pk_add_f32 v[16:17], v[16:17], v[32:33]
	v_max_f32_dpp v41, v41, v41 row_mirror row_mask:0xf bank_mask:0xf
	s_nop 1
	v_max_f32_dpp v41, v41, v41 row_bcast:15 row_mask:0xa bank_mask:0xf
	s_nop 1
	v_max_f32_dpp v41, v41, v41 row_bcast:31 row_mask:0xc bank_mask:0xf
	s_nop 1
	v_readlane_b32 s28, v41, 63
	s_nop 1
	v_div_scale_f32 v48, s[30:31], s28, s28, v47
	v_rcp_f32_e32 v49, v48
	s_nop 0
	v_fma_f32 v50, -v48, v49, 1.0
	v_fmac_f32_e32 v49, v50, v49
	v_mov_b32_e32 v50, s28
	v_div_scale_f32 v50, vcc, s32, v50, s32
	v_mul_f32_e32 v51, v50, v49
	v_fma_f32 v52, -v48, v51, v50
	v_fmac_f32_e32 v51, v52, v49
	v_fma_f32 v48, -v48, v51, v50
	v_div_fmas_f32 v48, v48, v49, v51
	v_div_fixup_f32 v48, v48, s28, v47
	v_cmp_gt_f32_e64 vcc, s28, 0
	v_writelane_b32 v40, s28, 17
	s_nop 0
	v_cndmask_b32_e32 v48, 0, v48, vcc
	v_fmaak_f32 v49, v18, v48, 0x4b400000
	v_fmaak_f32 v50, v19, v48, 0x4b400000
	v_fmaak_f32 v51, v20, v48, 0x4b400000
	v_fmaak_f32 v52, v21, v48, 0x4b400000
	v_perm_b32 v49, v50, v49, s33
	v_perm_b32 v51, v52, v51, s34
	v_or_b32_e32 v124, v49, v51
	v_fmaak_f32 v41, v22, v48, 0x4b400000
	v_fmaak_f32 v42, v23, v48, 0x4b400000
	v_fmaak_f32 v43, v24, v48, 0x4b400000
	v_fmaak_f32 v44, v25, v48, 0x4b400000
	v_perm_b32 v41, v42, v41, s33
	v_perm_b32 v43, v44, v43, s34
	v_or_b32_e32 v125, v41, v43
	v_fmaak_f32 v49, v26, v48, 0x4b400000
	v_fmaak_f32 v50, v27, v48, 0x4b400000
	v_fmaak_f32 v51, v28, v48, 0x4b400000
	v_fmaak_f32 v52, v29, v48, 0x4b400000
	v_perm_b32 v49, v50, v49, s33
	v_perm_b32 v51, v52, v51, s34
	v_or_b32_e32 v126, v49, v51
	v_fmaak_f32 v41, v30, v48, 0x4b400000
	v_fmaak_f32 v42, v31, v48, 0x4b400000
	v_fmaak_f32 v43, v32, v48, 0x4b400000
	v_fmaak_f32 v44, v33, v48, 0x4b400000
	v_perm_b32 v41, v42, v41, s33
	v_perm_b32 v43, v44, v43, s34
	v_or_b32_e32 v127, v41, v43
	s_waitcnt vmcnt(0)
	ds_read_b128 v[18:21], v38 offset:0
	ds_read_b128 v[22:25], v38 offset:1024
	ds_read_b128 v[26:29], v38 offset:2048
	ds_read_b128 v[30:33], v38 offset:3072
	s_waitcnt lgkmcnt(0)
	s_mov_b32 m0, s36
	s_nop 0
	global_load_lds_dwordx4 v34, s[16:17] nt
	global_load_lds_dwordx4 v34, s[16:17] offset:1024 nt
	global_load_lds_dwordx4 v34, s[16:17] offset:2048 nt
	global_load_lds_dwordx4 v35, s[16:17] offset:3072 nt
	s_add_u32 s16, s16, 0xfa0000
	s_addc_u32 s17, s17, 0
	v_cndmask_b32_e64 v30, 0, v30, s[18:19]
	v_cndmask_b32_e64 v31, 0, v31, s[18:19]
	v_cndmask_b32_e64 v32, 0, v32, s[18:19]
	v_cndmask_b32_e64 v33, 0, v33, s[18:19]
	v_max3_f32 v41, |v18|, |v19|, |v20|
	v_max3_f32 v42, |v21|, |v22|, |v23|
	v_max3_f32 v43, |v24|, |v25|, |v26|
	v_max3_f32 v44, |v27|, |v28|, |v29|
	v_max3_f32 v48, |v30|, |v31|, |v32|
	v_max3_f32 v41, v41, v42, |v33|
	v_max3_f32 v43, v43, v44, v48
	v_max_f32_e32 v41, v41, v43
	v_pk_add_f32 v[2:3], v[2:3], v[18:19]
	v_pk_add_f32 v[4:5], v[4:5], v[20:21]
	v_max_f32_dpp v41, v41, v41 quad_perm:[1,0,3,2] row_mask:0xf bank_mask:0xf
	v_pk_add_f32 v[6:7], v[6:7], v[22:23]
	v_pk_add_f32 v[8:9], v[8:9], v[24:25]
	v_max_f32_dpp v41, v41, v41 quad_perm:[2,3,0,1] row_mask:0xf bank_mask:0xf
	v_pk_add_f32 v[10:11], v[10:11], v[26:27]
	v_pk_add_f32 v[12:13], v[12:13], v[28:29]
	v_max_f32_dpp v41, v41, v41 row_half_mirror row_mask:0xf bank_mask:0xf
	v_pk_add_f32 v[14:15], v[14:15], v[30:31]
	v_pk_add_f32 v[16:17], v[16:17], v[32:33]
	v_max_f32_dpp v41, v41, v41 row_mirror row_mask:0xf bank_mask:0xf
	s_nop 1
	v_max_f32_dpp v41, v41, v41 row_bcast:15 row_mask:0xa bank_mask:0xf
	s_nop 1
	v_max_f32_dpp v41, v41, v41 row_bcast:31 row_mask:0xc bank_mask:0xf
	s_nop 1
	v_readlane_b32 s28, v41, 63
	s_nop 1
	v_div_scale_f32 v48, s[30:31], s28, s28, v47
	v_rcp_f32_e32 v49, v48
	s_nop 0
	v_fma_f32 v50, -v48, v49, 1.0
	v_fmac_f32_e32 v49, v50, v49
	v_mov_b32_e32 v50, s28
	v_div_scale_f32 v50, vcc, s32, v50, s32
	v_mul_f32_e32 v51, v50, v49
	v_fma_f32 v52, -v48, v51, v50
	v_fmac_f32_e32 v51, v52, v49
	v_fma_f32 v48, -v48, v51, v50
	v_div_fmas_f32 v48, v48, v49, v51
	v_div_fixup_f32 v48, v48, s28, v47
	v_cmp_gt_f32_e64 vcc, s28, 0
	v_writelane_b32 v40, s28, 18
	s_nop 0
	v_cndmask_b32_e32 v48, 0, v48, vcc
	v_fmaak_f32 v49, v18, v48, 0x4b400000
	v_fmaak_f32 v50, v19, v48, 0x4b400000
	v_fmaak_f32 v51, v20, v48, 0x4b400000
	v_fmaak_f32 v52, v21, v48, 0x4b400000
	v_perm_b32 v49, v50, v49, s33
	v_perm_b32 v51, v52, v51, s34
	v_or_b32_e32 v49, v49, v51
	s_add_u32 s20, s20, 0x900000
	s_addc_u32 s21, s21, 0
	s_add_u32 s22, s22, 0x900000
	s_addc_u32 s23, s23, 0
	s_add_u32 s24, s24, 0x900000
	s_addc_u32 s25, s25, 0
	s_add_u32 s26, s26, 0x900000
	s_addc_u32 s27, s27, 0
	global_store_dword v39, v49, s[20:21]
	v_fmaak_f32 v41, v22, v48, 0x4b400000
	v_fmaak_f32 v42, v23, v48, 0x4b400000
	v_fmaak_f32 v43, v24, v48, 0x4b400000
	v_fmaak_f32 v44, v25, v48, 0x4b400000
	v_perm_b32 v41, v42, v41, s33
	v_perm_b32 v43, v44, v43, s34
	v_or_b32_e32 v41, v41, v43
	global_store_dword v39, v41, s[22:23]
	v_fmaak_f32 v49, v26, v48, 0x4b400000
	v_fmaak_f32 v50, v27, v48, 0x4b400000
	v_fmaak_f32 v51, v28, v48, 0x4b400000
	v_fmaak_f32 v52, v29, v48, 0x4b400000
	v_perm_b32 v49, v50, v49, s33
	v_perm_b32 v51, v52, v51, s34
	v_or_b32_e32 v49, v49, v51
	global_store_dword v39, v49, s[24:25]
	v_fmaak_f32 v41, v30, v48, 0x4b400000
	v_fmaak_f32 v42, v31, v48, 0x4b400000
	v_fmaak_f32 v43, v32, v48, 0x4b400000
	v_fmaak_f32 v44, v33, v48, 0x4b400000
	v_perm_b32 v41, v42, v41, s33
	v_perm_b32 v43, v44, v43, s34
	v_or_b32_e32 v41, v41, v43
	global_store_dword v39, v41, s[26:27]
	s_waitcnt vmcnt(4)
	ds_read_b128 v[18:21], v38 offset:4096
	ds_read_b128 v[22:25], v38 offset:5120
	ds_read_b128 v[26:29], v38 offset:6144
	ds_read_b128 v[30:33], v38 offset:7168
	s_waitcnt lgkmcnt(0)
	s_mov_b32 m0, s35
	s_nop 0
	global_load_lds_dwordx4 v34, s[16:17] nt
	global_load_lds_dwordx4 v34, s[16:17] offset:1024 nt
	global_load_lds_dwordx4 v34, s[16:17] offset:2048 nt
	global_load_lds_dwordx4 v35, s[16:17] offset:3072 nt
	s_add_u32 s16, s16, 0xfa0000
	s_addc_u32 s17, s17, 0
	v_cndmask_b32_e64 v30, 0, v30, s[18:19]
	v_cndmask_b32_e64 v31, 0, v31, s[18:19]
	v_cndmask_b32_e64 v32, 0, v32, s[18:19]
	v_cndmask_b32_e64 v33, 0, v33, s[18:19]
	v_max3_f32 v41, |v18|, |v19|, |v20|
	v_max3_f32 v42, |v21|, |v22|, |v23|
	v_max3_f32 v43, |v24|, |v25|, |v26|
	v_max3_f32 v44, |v27|, |v28|, |v29|
	v_max3_f32 v48, |v30|, |v31|, |v32|
	v_max3_f32 v41, v41, v42, |v33|
	v_max3_f32 v43, v43, v44, v48
	v_max_f32_e32 v41, v41, v43
	v_pk_add_f32 v[2:3], v[2:3], v[18:19]
	v_pk_add_f32 v[4:5], v[4:5], v[20:21]
	v_max_f32_dpp v41, v41, v41 quad_perm:[1,0,3,2] row_mask:0xf bank_mask:0xf
	v_pk_add_f32 v[6:7], v[6:7], v[22:23]
	v_pk_add_f32 v[8:9], v[8:9], v[24:25]
	v_max_f32_dpp v41, v41, v41 quad_perm:[2,3,0,1] row_mask:0xf bank_mask:0xf
	v_pk_add_f32 v[10:11], v[10:11], v[26:27]
	v_pk_add_f32 v[12:13], v[12:13], v[28:29]
	v_max_f32_dpp v41, v41, v41 row_half_mirror row_mask:0xf bank_mask:0xf
	v_pk_add_f32 v[14:15], v[14:15], v[30:31]
	v_pk_add_f32 v[16:17], v[16:17], v[32:33]
	v_max_f32_dpp v41, v41, v41 row_mirror row_mask:0xf bank_mask:0xf
	s_nop 1
	v_max_f32_dpp v41, v41, v41 row_bcast:15 row_mask:0xa bank_mask:0xf
	s_nop 1
	v_max_f32_dpp v41, v41, v41 row_bcast:31 row_mask:0xc bank_mask:0xf
	s_nop 1
	v_readlane_b32 s28, v41, 63
	s_nop 1
	v_div_scale_f32 v48, s[30:31], s28, s28, v47
	v_rcp_f32_e32 v49, v48
	s_nop 0
	v_fma_f32 v50, -v48, v49, 1.0
	v_fmac_f32_e32 v49, v50, v49
	v_mov_b32_e32 v50, s28
	v_div_scale_f32 v50, vcc, s32, v50, s32
	v_mul_f32_e32 v51, v50, v49
	v_fma_f32 v52, -v48, v51, v50
	v_fmac_f32_e32 v51, v52, v49
	v_fma_f32 v48, -v48, v51, v50
	v_div_fmas_f32 v48, v48, v49, v51
	v_div_fixup_f32 v48, v48, s28, v47
	v_cmp_gt_f32_e64 vcc, s28, 0
	v_writelane_b32 v40, s28, 19
	s_nop 0
	v_cndmask_b32_e32 v48, 0, v48, vcc
	v_fmaak_f32 v49, v18, v48, 0x4b400000
	v_fmaak_f32 v50, v19, v48, 0x4b400000
	v_fmaak_f32 v51, v20, v48, 0x4b400000
	v_fmaak_f32 v52, v21, v48, 0x4b400000
	v_perm_b32 v49, v50, v49, s33
	v_perm_b32 v51, v52, v51, s34
	v_or_b32_e32 v49, v49, v51
	s_add_u32 s20, s20, 0x80000
	s_addc_u32 s21, s21, 0
	s_add_u32 s22, s22, 0x80000
	s_addc_u32 s23, s23, 0
	s_add_u32 s24, s24, 0x80000
	s_addc_u32 s25, s25, 0
	s_add_u32 s26, s26, 0x80000
	s_addc_u32 s27, s27, 0
	global_store_dword v39, v49, s[20:21]
	v_fmaak_f32 v41, v22, v48, 0x4b400000
	v_fmaak_f32 v42, v23, v48, 0x4b400000
	v_fmaak_f32 v43, v24, v48, 0x4b400000
	v_fmaak_f32 v44, v25, v48, 0x4b400000
	v_perm_b32 v41, v42, v41, s33
	v_perm_b32 v43, v44, v43, s34
	v_or_b32_e32 v41, v41, v43
	global_store_dword v39, v41, s[22:23]
	v_fmaak_f32 v49, v26, v48, 0x4b400000
	v_fmaak_f32 v50, v27, v48, 0x4b400000
	v_fmaak_f32 v51, v28, v48, 0x4b400000
	v_fmaak_f32 v52, v29, v48, 0x4b400000
	v_perm_b32 v49, v50, v49, s33
	v_perm_b32 v51, v52, v51, s34
	v_or_b32_e32 v49, v49, v51
	global_store_dword v39, v49, s[24:25]
	v_fmaak_f32 v41, v30, v48, 0x4b400000
	v_fmaak_f32 v42, v31, v48, 0x4b400000
	v_fmaak_f32 v43, v32, v48, 0x4b400000
	v_fmaak_f32 v44, v33, v48, 0x4b400000
	v_perm_b32 v41, v42, v41, s33
	v_perm_b32 v43, v44, v43, s34
	v_or_b32_e32 v41, v41, v43
	global_store_dword v39, v41, s[26:27]
	s_waitcnt vmcnt(4)
	ds_read_b128 v[18:21], v38 offset:0
	ds_read_b128 v[22:25], v38 offset:1024
	ds_read_b128 v[26:29], v38 offset:2048
	ds_read_b128 v[30:33], v38 offset:3072
	s_waitcnt lgkmcnt(0)
	s_mov_b32 m0, s36
	s_nop 0
	global_load_lds_dwordx4 v34, s[16:17] nt
	global_load_lds_dwordx4 v34, s[16:17] offset:1024 nt
	global_load_lds_dwordx4 v34, s[16:17] offset:2048 nt
	global_load_lds_dwordx4 v35, s[16:17] offset:3072 nt
	s_add_u32 s16, s16, 0xfa0000
	s_addc_u32 s17, s17, 0
	v_cndmask_b32_e64 v30, 0, v30, s[18:19]
	v_cndmask_b32_e64 v31, 0, v31, s[18:19]
	v_cndmask_b32_e64 v32, 0, v32, s[18:19]
	v_cndmask_b32_e64 v33, 0, v33, s[18:19]
	v_max3_f32 v41, |v18|, |v19|, |v20|
	v_max3_f32 v42, |v21|, |v22|, |v23|
	v_max3_f32 v43, |v24|, |v25|, |v26|
	v_max3_f32 v44, |v27|, |v28|, |v29|
	v_max3_f32 v48, |v30|, |v31|, |v32|
	v_max3_f32 v41, v41, v42, |v33|
	v_max3_f32 v43, v43, v44, v48
	v_max_f32_e32 v41, v41, v43
	v_pk_add_f32 v[2:3], v[2:3], v[18:19]
	v_pk_add_f32 v[4:5], v[4:5], v[20:21]
	v_max_f32_dpp v41, v41, v41 quad_perm:[1,0,3,2] row_mask:0xf bank_mask:0xf
	v_pk_add_f32 v[6:7], v[6:7], v[22:23]
	v_pk_add_f32 v[8:9], v[8:9], v[24:25]
	v_max_f32_dpp v41, v41, v41 quad_perm:[2,3,0,1] row_mask:0xf bank_mask:0xf
	v_pk_add_f32 v[10:11], v[10:11], v[26:27]
	v_pk_add_f32 v[12:13], v[12:13], v[28:29]
	v_max_f32_dpp v41, v41, v41 row_half_mirror row_mask:0xf bank_mask:0xf
	v_pk_add_f32 v[14:15], v[14:15], v[30:31]
	v_pk_add_f32 v[16:17], v[16:17], v[32:33]
	v_max_f32_dpp v41, v41, v41 row_mirror row_mask:0xf bank_mask:0xf
	s_nop 1
	v_max_f32_dpp v41, v41, v41 row_bcast:15 row_mask:0xa bank_mask:0xf
	s_nop 1
	v_max_f32_dpp v41, v41, v41 row_bcast:31 row_mask:0xc bank_mask:0xf
	s_nop 1
	v_readlane_b32 s28, v41, 63
	s_nop 1
	v_div_scale_f32 v48, s[30:31], s28, s28, v47
	v_rcp_f32_e32 v49, v48
	s_nop 0
	v_fma_f32 v50, -v48, v49, 1.0
	v_fmac_f32_e32 v49, v50, v49
	v_mov_b32_e32 v50, s28
	v_div_scale_f32 v50, vcc, s32, v50, s32
	v_mul_f32_e32 v51, v50, v49
	v_fma_f32 v52, -v48, v51, v50
	v_fmac_f32_e32 v51, v52, v49
	v_fma_f32 v48, -v48, v51, v50
	v_div_fmas_f32 v48, v48, v49, v51
	v_div_fixup_f32 v48, v48, s28, v47
	v_cmp_gt_f32_e64 vcc, s28, 0
	v_writelane_b32 v40, s28, 20
	s_nop 0
	v_cndmask_b32_e32 v48, 0, v48, vcc
	v_fmaak_f32 v49, v18, v48, 0x4b400000
	v_fmaak_f32 v50, v19, v48, 0x4b400000
	v_fmaak_f32 v51, v20, v48, 0x4b400000
	v_fmaak_f32 v52, v21, v48, 0x4b400000
	v_perm_b32 v49, v50, v49, s33
	v_perm_b32 v51, v52, v51, s34
	v_or_b32_e32 v49, v49, v51
	s_add_u32 s20, s20, 0x80000
	s_addc_u32 s21, s21, 0
	s_add_u32 s22, s22, 0x80000
	s_addc_u32 s23, s23, 0
	s_add_u32 s24, s24, 0x80000
	s_addc_u32 s25, s25, 0
	s_add_u32 s26, s26, 0x80000
	s_addc_u32 s27, s27, 0
	global_store_dword v39, v49, s[20:21]
	v_fmaak_f32 v41, v22, v48, 0x4b400000
	v_fmaak_f32 v42, v23, v48, 0x4b400000
	v_fmaak_f32 v43, v24, v48, 0x4b400000
	v_fmaak_f32 v44, v25, v48, 0x4b400000
	v_perm_b32 v41, v42, v41, s33
	v_perm_b32 v43, v44, v43, s34
	v_or_b32_e32 v41, v41, v43
	global_store_dword v39, v41, s[22:23]
	v_fmaak_f32 v49, v26, v48, 0x4b400000
	v_fmaak_f32 v50, v27, v48, 0x4b400000
	v_fmaak_f32 v51, v28, v48, 0x4b400000
	v_fmaak_f32 v52, v29, v48, 0x4b400000
	v_perm_b32 v49, v50, v49, s33
	v_perm_b32 v51, v52, v51, s34
	v_or_b32_e32 v49, v49, v51
	global_store_dword v39, v49, s[24:25]
	v_fmaak_f32 v41, v30, v48, 0x4b400000
	v_fmaak_f32 v42, v31, v48, 0x4b400000
	v_fmaak_f32 v43, v32, v48, 0x4b400000
	v_fmaak_f32 v44, v33, v48, 0x4b400000
	v_perm_b32 v41, v42, v41, s33
	v_perm_b32 v43, v44, v43, s34
	v_or_b32_e32 v41, v41, v43
	global_store_dword v39, v41, s[26:27]
	s_waitcnt vmcnt(4)
	ds_read_b128 v[18:21], v38 offset:4096
	ds_read_b128 v[22:25], v38 offset:5120
	ds_read_b128 v[26:29], v38 offset:6144
	ds_read_b128 v[30:33], v38 offset:7168
	s_waitcnt lgkmcnt(0)
	s_mov_b32 m0, s35
	s_nop 0
	global_load_lds_dwordx4 v34, s[16:17] nt
	global_load_lds_dwordx4 v34, s[16:17] offset:1024 nt
	global_load_lds_dwordx4 v34, s[16:17] offset:2048 nt
	global_load_lds_dwordx4 v35, s[16:17] offset:3072 nt
	s_add_u32 s16, s16, 0xfa0000
	s_addc_u32 s17, s17, 0
	v_cndmask_b32_e64 v30, 0, v30, s[18:19]
	v_cndmask_b32_e64 v31, 0, v31, s[18:19]
	v_cndmask_b32_e64 v32, 0, v32, s[18:19]
	v_cndmask_b32_e64 v33, 0, v33, s[18:19]
	v_max3_f32 v41, |v18|, |v19|, |v20|
	v_max3_f32 v42, |v21|, |v22|, |v23|
	v_max3_f32 v43, |v24|, |v25|, |v26|
	v_max3_f32 v44, |v27|, |v28|, |v29|
	v_max3_f32 v48, |v30|, |v31|, |v32|
	v_max3_f32 v41, v41, v42, |v33|
	v_max3_f32 v43, v43, v44, v48
	v_max_f32_e32 v41, v41, v43
	v_pk_add_f32 v[2:3], v[2:3], v[18:19]
	v_pk_add_f32 v[4:5], v[4:5], v[20:21]
	v_max_f32_dpp v41, v41, v41 quad_perm:[1,0,3,2] row_mask:0xf bank_mask:0xf
	v_pk_add_f32 v[6:7], v[6:7], v[22:23]
	v_pk_add_f32 v[8:9], v[8:9], v[24:25]
	v_max_f32_dpp v41, v41, v41 quad_perm:[2,3,0,1] row_mask:0xf bank_mask:0xf
	v_pk_add_f32 v[10:11], v[10:11], v[26:27]
	v_pk_add_f32 v[12:13], v[12:13], v[28:29]
	v_max_f32_dpp v41, v41, v41 row_half_mirror row_mask:0xf bank_mask:0xf
	v_pk_add_f32 v[14:15], v[14:15], v[30:31]
	v_pk_add_f32 v[16:17], v[16:17], v[32:33]
	v_max_f32_dpp v41, v41, v41 row_mirror row_mask:0xf bank_mask:0xf
	s_nop 1
	v_max_f32_dpp v41, v41, v41 row_bcast:15 row_mask:0xa bank_mask:0xf
	s_nop 1
	v_max_f32_dpp v41, v41, v41 row_bcast:31 row_mask:0xc bank_mask:0xf
	s_nop 1
	v_readlane_b32 s28, v41, 63
	s_nop 1
	v_div_scale_f32 v48, s[30:31], s28, s28, v47
	v_rcp_f32_e32 v49, v48
	s_nop 0
	v_fma_f32 v50, -v48, v49, 1.0
	v_fmac_f32_e32 v49, v50, v49
	v_mov_b32_e32 v50, s28
	v_div_scale_f32 v50, vcc, s32, v50, s32
	v_mul_f32_e32 v51, v50, v49
	v_fma_f32 v52, -v48, v51, v50
	v_fmac_f32_e32 v51, v52, v49
	v_fma_f32 v48, -v48, v51, v50
	v_div_fmas_f32 v48, v48, v49, v51
	v_div_fixup_f32 v48, v48, s28, v47
	v_cmp_gt_f32_e64 vcc, s28, 0
	v_writelane_b32 v40, s28, 21
	s_nop 0
	v_cndmask_b32_e32 v48, 0, v48, vcc
	v_fmaak_f32 v49, v18, v48, 0x4b400000
	v_fmaak_f32 v50, v19, v48, 0x4b400000
	v_fmaak_f32 v51, v20, v48, 0x4b400000
	v_fmaak_f32 v52, v21, v48, 0x4b400000
	v_perm_b32 v49, v50, v49, s33
	v_perm_b32 v51, v52, v51, s34
	v_or_b32_e32 v49, v49, v51
	s_add_u32 s20, s20, 0x80000
	s_addc_u32 s21, s21, 0
	s_add_u32 s22, s22, 0x80000
	s_addc_u32 s23, s23, 0
	s_add_u32 s24, s24, 0x80000
	s_addc_u32 s25, s25, 0
	s_add_u32 s26, s26, 0x80000
	s_addc_u32 s27, s27, 0
	global_store_dword v39, v49, s[20:21]
	v_fmaak_f32 v41, v22, v48, 0x4b400000
	v_fmaak_f32 v42, v23, v48, 0x4b400000
	v_fmaak_f32 v43, v24, v48, 0x4b400000
	v_fmaak_f32 v44, v25, v48, 0x4b400000
	v_perm_b32 v41, v42, v41, s33
	v_perm_b32 v43, v44, v43, s34
	v_or_b32_e32 v41, v41, v43
	global_store_dword v39, v41, s[22:23]
	v_fmaak_f32 v49, v26, v48, 0x4b400000
	v_fmaak_f32 v50, v27, v48, 0x4b400000
	v_fmaak_f32 v51, v28, v48, 0x4b400000
	v_fmaak_f32 v52, v29, v48, 0x4b400000
	v_perm_b32 v49, v50, v49, s33
	v_perm_b32 v51, v52, v51, s34
	v_or_b32_e32 v49, v49, v51
	global_store_dword v39, v49, s[24:25]
	v_fmaak_f32 v41, v30, v48, 0x4b400000
	v_fmaak_f32 v42, v31, v48, 0x4b400000
	v_fmaak_f32 v43, v32, v48, 0x4b400000
	v_fmaak_f32 v44, v33, v48, 0x4b400000
	v_perm_b32 v41, v42, v41, s33
	v_perm_b32 v43, v44, v43, s34
	v_or_b32_e32 v41, v41, v43
	global_store_dword v39, v41, s[26:27]
	s_waitcnt vmcnt(4)
	ds_read_b128 v[18:21], v38 offset:0
	ds_read_b128 v[22:25], v38 offset:1024
	ds_read_b128 v[26:29], v38 offset:2048
	ds_read_b128 v[30:33], v38 offset:3072
	s_waitcnt lgkmcnt(0)
	s_mov_b32 m0, s36
	s_nop 0
	global_load_lds_dwordx4 v34, s[16:17] nt
	global_load_lds_dwordx4 v34, s[16:17] offset:1024 nt
	global_load_lds_dwordx4 v34, s[16:17] offset:2048 nt
	global_load_lds_dwordx4 v35, s[16:17] offset:3072 nt
	s_add_u32 s16, s16, 0xfa0000
	s_addc_u32 s17, s17, 0
	v_cndmask_b32_e64 v30, 0, v30, s[18:19]
	v_cndmask_b32_e64 v31, 0, v31, s[18:19]
	v_cndmask_b32_e64 v32, 0, v32, s[18:19]
	v_cndmask_b32_e64 v33, 0, v33, s[18:19]
	v_max3_f32 v41, |v18|, |v19|, |v20|
	v_max3_f32 v42, |v21|, |v22|, |v23|
	v_max3_f32 v43, |v24|, |v25|, |v26|
	v_max3_f32 v44, |v27|, |v28|, |v29|
	v_max3_f32 v48, |v30|, |v31|, |v32|
	v_max3_f32 v41, v41, v42, |v33|
	v_max3_f32 v43, v43, v44, v48
	v_max_f32_e32 v41, v41, v43
	v_pk_add_f32 v[2:3], v[2:3], v[18:19]
	v_pk_add_f32 v[4:5], v[4:5], v[20:21]
	v_max_f32_dpp v41, v41, v41 quad_perm:[1,0,3,2] row_mask:0xf bank_mask:0xf
	v_pk_add_f32 v[6:7], v[6:7], v[22:23]
	v_pk_add_f32 v[8:9], v[8:9], v[24:25]
	v_max_f32_dpp v41, v41, v41 quad_perm:[2,3,0,1] row_mask:0xf bank_mask:0xf
	v_pk_add_f32 v[10:11], v[10:11], v[26:27]
	v_pk_add_f32 v[12:13], v[12:13], v[28:29]
	v_max_f32_dpp v41, v41, v41 row_half_mirror row_mask:0xf bank_mask:0xf
	v_pk_add_f32 v[14:15], v[14:15], v[30:31]
	v_pk_add_f32 v[16:17], v[16:17], v[32:33]
	v_max_f32_dpp v41, v41, v41 row_mirror row_mask:0xf bank_mask:0xf
	s_nop 1
	v_max_f32_dpp v41, v41, v41 row_bcast:15 row_mask:0xa bank_mask:0xf
	s_nop 1
	v_max_f32_dpp v41, v41, v41 row_bcast:31 row_mask:0xc bank_mask:0xf
	s_nop 1
	v_readlane_b32 s28, v41, 63
	s_nop 1
	v_div_scale_f32 v48, s[30:31], s28, s28, v47
	v_rcp_f32_e32 v49, v48
	s_nop 0
	v_fma_f32 v50, -v48, v49, 1.0
	v_fmac_f32_e32 v49, v50, v49
	v_mov_b32_e32 v50, s28
	v_div_scale_f32 v50, vcc, s32, v50, s32
	v_mul_f32_e32 v51, v50, v49
	v_fma_f32 v52, -v48, v51, v50
	v_fmac_f32_e32 v51, v52, v49
	v_fma_f32 v48, -v48, v51, v50
	v_div_fmas_f32 v48, v48, v49, v51
	v_div_fixup_f32 v48, v48, s28, v47
	v_cmp_gt_f32_e64 vcc, s28, 0
	v_writelane_b32 v40, s28, 22
	s_nop 0
	v_cndmask_b32_e32 v48, 0, v48, vcc
	v_fmaak_f32 v49, v18, v48, 0x4b400000
	v_fmaak_f32 v50, v19, v48, 0x4b400000
	v_fmaak_f32 v51, v20, v48, 0x4b400000
	v_fmaak_f32 v52, v21, v48, 0x4b400000
	v_perm_b32 v49, v50, v49, s33
	v_perm_b32 v51, v52, v51, s34
	v_or_b32_e32 v49, v49, v51
	s_add_u32 s20, s20, 0x80000
	s_addc_u32 s21, s21, 0
	s_add_u32 s22, s22, 0x80000
	s_addc_u32 s23, s23, 0
	s_add_u32 s24, s24, 0x80000
	s_addc_u32 s25, s25, 0
	s_add_u32 s26, s26, 0x80000
	s_addc_u32 s27, s27, 0
	global_store_dword v39, v49, s[20:21]
	v_fmaak_f32 v41, v22, v48, 0x4b400000
	v_fmaak_f32 v42, v23, v48, 0x4b400000
	v_fmaak_f32 v43, v24, v48, 0x4b400000
	v_fmaak_f32 v44, v25, v48, 0x4b400000
	v_perm_b32 v41, v42, v41, s33
	v_perm_b32 v43, v44, v43, s34
	v_or_b32_e32 v41, v41, v43
	global_store_dword v39, v41, s[22:23]
	v_fmaak_f32 v49, v26, v48, 0x4b400000
	v_fmaak_f32 v50, v27, v48, 0x4b400000
	v_fmaak_f32 v51, v28, v48, 0x4b400000
	v_fmaak_f32 v52, v29, v48, 0x4b400000
	v_perm_b32 v49, v50, v49, s33
	v_perm_b32 v51, v52, v51, s34
	v_or_b32_e32 v49, v49, v51
	global_store_dword v39, v49, s[24:25]
	v_fmaak_f32 v41, v30, v48, 0x4b400000
	v_fmaak_f32 v42, v31, v48, 0x4b400000
	v_fmaak_f32 v43, v32, v48, 0x4b400000
	v_fmaak_f32 v44, v33, v48, 0x4b400000
	v_perm_b32 v41, v42, v41, s33
	v_perm_b32 v43, v44, v43, s34
	v_or_b32_e32 v41, v41, v43
	global_store_dword v39, v41, s[26:27]
	s_waitcnt vmcnt(4)
	ds_read_b128 v[18:21], v38 offset:4096
	ds_read_b128 v[22:25], v38 offset:5120
	ds_read_b128 v[26:29], v38 offset:6144
	ds_read_b128 v[30:33], v38 offset:7168
	s_waitcnt lgkmcnt(0)
	s_cmp_eq_u32 s29, 1
	s_cbranch_scc0 .Lk1_nodma24
	s_mov_b32 m0, s35
	s_nop 0
	global_load_lds_dwordx4 v34, s[16:17] nt
	global_load_lds_dwordx4 v34, s[16:17] offset:1024 nt
	global_load_lds_dwordx4 v34, s[16:17] offset:2048 nt
	global_load_lds_dwordx4 v35, s[16:17] offset:3072 nt
	s_add_u32 s16, s16, 0xfa0000
	s_addc_u32 s17, s17, 0
.Lk1_nodma24:
	v_cndmask_b32_e64 v30, 0, v30, s[18:19]
	v_cndmask_b32_e64 v31, 0, v31, s[18:19]
	v_cndmask_b32_e64 v32, 0, v32, s[18:19]
	v_cndmask_b32_e64 v33, 0, v33, s[18:19]
	v_max3_f32 v41, |v18|, |v19|, |v20|
	v_max3_f32 v42, |v21|, |v22|, |v23|
	v_max3_f32 v43, |v24|, |v25|, |v26|
	v_max3_f32 v44, |v27|, |v28|, |v29|
	v_max3_f32 v48, |v30|, |v31|, |v32|
	v_max3_f32 v41, v41, v42, |v33|
	v_max3_f32 v43, v43, v44, v48
	v_max_f32_e32 v41, v41, v43
	v_pk_add_f32 v[2:3], v[2:3], v[18:19]
	v_pk_add_f32 v[4:5], v[4:5], v[20:21]
	v_max_f32_dpp v41, v41, v41 quad_perm:[1,0,3,2] row_mask:0xf bank_mask:0xf
	v_pk_add_f32 v[6:7], v[6:7], v[22:23]
	v_pk_add_f32 v[8:9], v[8:9], v[24:25]
	v_max_f32_dpp v41, v41, v41 quad_perm:[2,3,0,1] row_mask:0xf bank_mask:0xf
	v_pk_add_f32 v[10:11], v[10:11], v[26:27]
	v_pk_add_f32 v[12:13], v[12:13], v[28:29]
	v_max_f32_dpp v41, v41, v41 row_half_mirror row_mask:0xf bank_mask:0xf
	v_pk_add_f32 v[14:15], v[14:15], v[30:31]
	v_pk_add_f32 v[16:17], v[16:17], v[32:33]
	v_max_f32_dpp v41, v41, v41 row_mirror row_mask:0xf bank_mask:0xf
	s_nop 1
	v_max_f32_dpp v41, v41, v41 row_bcast:15 row_mask:0xa bank_mask:0xf
	s_nop 1
	v_max_f32_dpp v41, v41, v41 row_bcast:31 row_mask:0xc bank_mask:0xf
	s_nop 1
	v_readlane_b32 s28, v41, 63
	s_nop 1
	v_div_scale_f32 v48, s[30:31], s28, s28, v47
	v_rcp_f32_e32 v49, v48
	s_nop 0
	v_fma_f32 v50, -v48, v49, 1.0
	v_fmac_f32_e32 v49, v50, v49
	v_mov_b32_e32 v50, s28
	v_div_scale_f32 v50, vcc, s32, v50, s32
	v_mul_f32_e32 v51, v50, v49
	v_fma_f32 v52, -v48, v51, v50
	v_fmac_f32_e32 v51, v52, v49
	v_fma_f32 v48, -v48, v51, v50
	v_div_fmas_f32 v48, v48, v49, v51
	v_div_fixup_f32 v48, v48, s28, v47
	v_cmp_gt_f32_e64 vcc, s28, 0
	v_writelane_b32 v40, s28, 23
	s_nop 0
	v_cndmask_b32_e32 v48, 0, v48, vcc
	v_fmaak_f32 v49, v18, v48, 0x4b400000
	v_fmaak_f32 v50, v19, v48, 0x4b400000
	v_fmaak_f32 v51, v20, v48, 0x4b400000
	v_fmaak_f32 v52, v21, v48, 0x4b400000
	v_perm_b32 v49, v50, v49, s33
	v_perm_b32 v51, v52, v51, s34
	v_or_b32_e32 v49, v49, v51
	s_add_u32 s20, s20, 0x80000
	s_addc_u32 s21, s21, 0
	s_add_u32 s22, s22, 0x80000
	s_addc_u32 s23, s23, 0
	s_add_u32 s24, s24, 0x80000
	s_addc_u32 s25, s25, 0
	s_add_u32 s26, s26, 0x80000
	s_addc_u32 s27, s27, 0
	global_store_dword v39, v49, s[20:21]
	v_fmaak_f32 v41, v22, v48, 0x4b400000
	v_fmaak_f32 v42, v23, v48, 0x4b400000
	v_fmaak_f32 v43, v24, v48, 0x4b400000
	v_fmaak_f32 v44, v25, v48, 0x4b400000
	v_perm_b32 v41, v42, v41, s33
	v_perm_b32 v43, v44, v43, s34
	v_or_b32_e32 v41, v41, v43
	global_store_dword v39, v41, s[22:23]
	v_fmaak_f32 v49, v26, v48, 0x4b400000
	v_fmaak_f32 v50, v27, v48, 0x4b400000
	v_fmaak_f32 v51, v28, v48, 0x4b400000
	v_fmaak_f32 v52, v29, v48, 0x4b400000
	v_perm_b32 v49, v50, v49, s33
	v_perm_b32 v51, v52, v51, s34
	v_or_b32_e32 v49, v49, v51
	global_store_dword v39, v49, s[24:25]
	v_fmaak_f32 v41, v30, v48, 0x4b400000
	v_fmaak_f32 v42, v31, v48, 0x4b400000
	v_fmaak_f32 v43, v32, v48, 0x4b400000
	v_fmaak_f32 v44, v33, v48, 0x4b400000
	v_perm_b32 v41, v42, v41, s33
	v_perm_b32 v43, v44, v43, s34
	v_or_b32_e32 v41, v41, v43
	global_store_dword v39, v41, s[26:27]
	s_cmp_eq_u32 s29, 1
	s_cbranch_scc0 .Lk1_flush
	s_waitcnt vmcnt(4)
	ds_read_b128 v[18:21], v38 offset:0
	ds_read_b128 v[22:25], v38 offset:1024
	ds_read_b128 v[26:29], v38 offset:2048
	ds_read_b128 v[30:33], v38 offset:3072
	s_waitcnt lgkmcnt(0)
	v_cndmask_b32_e64 v30, 0, v30, s[18:19]
	v_cndmask_b32_e64 v31, 0, v31, s[18:19]
	v_cndmask_b32_e64 v32, 0, v32, s[18:19]
	v_cndmask_b32_e64 v33, 0, v33, s[18:19]
	v_max3_f32 v41, |v18|, |v19|, |v20|
	v_max3_f32 v42, |v21|, |v22|, |v23|
	v_max3_f32 v43, |v24|, |v25|, |v26|
	v_max3_f32 v44, |v27|, |v28|, |v29|
	v_max3_f32 v48, |v30|, |v31|, |v32|
	v_max3_f32 v41, v41, v42, |v33|
	v_max3_f32 v43, v43, v44, v48
	v_max_f32_e32 v41, v41, v43
	v_pk_add_f32 v[2:3], v[2:3], v[18:19]
	v_pk_add_f32 v[4:5], v[4:5], v[20:21]
	v_max_f32_dpp v41, v41, v41 quad_perm:[1,0,3,2] row_mask:0xf bank_mask:0xf
	v_pk_add_f32 v[6:7], v[6:7], v[22:23]
	v_pk_add_f32 v[8:9], v[8:9], v[24:25]
	v_max_f32_dpp v41, v41, v41 quad_perm:[2,3,0,1] row_mask:0xf bank_mask:0xf
	v_pk_add_f32 v[10:11], v[10:11], v[26:27]
	v_pk_add_f32 v[12:13], v[12:13], v[28:29]
	v_max_f32_dpp v41, v41, v41 row_half_mirror row_mask:0xf bank_mask:0xf
	v_pk_add_f32 v[14:15], v[14:15], v[30:31]
	v_pk_add_f32 v[16:17], v[16:17], v[32:33]
	v_max_f32_dpp v41, v41, v41 row_mirror row_mask:0xf bank_mask:0xf
	s_nop 1
	v_max_f32_dpp v41, v41, v41 row_bcast:15 row_mask:0xa bank_mask:0xf
	s_nop 1
	v_max_f32_dpp v41, v41, v41 row_bcast:31 row_mask:0xc bank_mask:0xf
	s_nop 1
	v_readlane_b32 s28, v41, 63
	s_nop 1
	v_div_scale_f32 v48, s[30:31], s28, s28, v47
	v_rcp_f32_e32 v49, v48
	s_nop 0
	v_fma_f32 v50, -v48, v49, 1.0
	v_fmac_f32_e32 v49, v50, v49
	v_mov_b32_e32 v50, s28
	v_div_scale_f32 v50, vcc, s32, v50, s32
	v_mul_f32_e32 v51, v50, v49
	v_fma_f32 v52, -v48, v51, v50
	v_fmac_f32_e32 v51, v52, v49
	v_fma_f32 v48, -v48, v51, v50
	v_div_fmas_f32 v48, v48, v49, v51
	v_div_fixup_f32 v48, v48, s28, v47
	v_cmp_gt_f32_e64 vcc, s28, 0
	v_writelane_b32 v40, s28, 24
	s_nop 0
	v_cndmask_b32_e32 v48, 0, v48, vcc
	v_fmaak_f32 v49, v18, v48, 0x4b400000
	v_fmaak_f32 v50, v19, v48, 0x4b400000
	v_fmaak_f32 v51, v20, v48, 0x4b400000
	v_fmaak_f32 v52, v21, v48, 0x4b400000
	v_perm_b32 v49, v50, v49, s33
	v_perm_b32 v51, v52, v51, s34
	v_or_b32_e32 v49, v49, v51
	s_add_u32 s20, s20, 0x80000
	s_addc_u32 s21, s21, 0
	s_add_u32 s22, s22, 0x80000
	s_addc_u32 s23, s23, 0
	s_add_u32 s24, s24, 0x80000
	s_addc_u32 s25, s25, 0
	s_add_u32 s26, s26, 0x80000
	s_addc_u32 s27, s27, 0
	global_store_dword v39, v49, s[20:21]
	v_fmaak_f32 v41, v22, v48, 0x4b400000
	v_fmaak_f32 v42, v23, v48, 0x4b400000
	v_fmaak_f32 v43, v24, v48, 0x4b400000
	v_fmaak_f32 v44, v25, v48, 0x4b400000
	v_perm_b32 v41, v42, v41, s33
	v_perm_b32 v43, v44, v43, s34
	v_or_b32_e32 v41, v41, v43
	global_store_dword v39, v41, s[22:23]
	v_fmaak_f32 v49, v26, v48, 0x4b400000
	v_fmaak_f32 v50, v27, v48, 0x4b400000
	v_fmaak_f32 v51, v28, v48, 0x4b400000
	v_fmaak_f32 v52, v29, v48, 0x4b400000
	v_perm_b32 v49, v50, v49, s33
	v_perm_b32 v51, v52, v51, s34
	v_or_b32_e32 v49, v49, v51
	global_store_dword v39, v49, s[24:25]
	v_fmaak_f32 v41, v30, v48, 0x4b400000
	v_fmaak_f32 v42, v31, v48, 0x4b400000
	v_fmaak_f32 v43, v32, v48, 0x4b400000
	v_fmaak_f32 v44, v33, v48, 0x4b400000
	v_perm_b32 v41, v42, v41, s33
	v_perm_b32 v43, v44, v43, s34
	v_or_b32_e32 v41, v41, v43
	global_store_dword v39, v41, s[26:27]
.Lk1_flush:
	s_add_u32 s20, s40, 0x0
	s_addc_u32 s21, s41, 0
	s_add_u32 s22, s20, 0x186a000
	s_addc_u32 s23, s21, 0
	s_add_u32 s24, s22, 0x186a000
	s_addc_u32 s25, s23, 0
	s_add_u32 s26, s24, 0x186a000
	s_addc_u32 s27, s25, 0
	global_store_dword v39, v56, s[20:21] sc1
	global_store_dword v39, v57, s[22:23] sc1
	global_store_dword v39, v58, s[24:25] sc1
	global_store_dword v39, v59, s[26:27] sc1
	s_add_u32 s20, s20, 0x80000
	s_addc_u32 s21, s21, 0
	s_add_u32 s22, s22, 0x80000
	s_addc_u32 s23, s23, 0
	s_add_u32 s24, s24, 0x80000
	s_addc_u32 s25, s25, 0
	s_add_u32 s26, s26, 0x80000
	s_addc_u32 s27, s27, 0
	global_store_dword v39, v60, s[20:21] sc1
	global_store_dword v39, v61, s[22:23] sc1
	global_store_dword v39, v62, s[24:25] sc1
	global_store_dword v39, v63, s[26:27] sc1
	s_add_u32 s20, s20, 0x80000
	s_addc_u32 s21, s21, 0
	s_add_u32 s22, s22, 0x80000
	s_addc_u32 s23, s23, 0
	s_add_u32 s24, s24, 0x80000
	s_addc_u32 s25, s25, 0
	s_add_u32 s26, s26, 0x80000
	s_addc_u32 s27, s27, 0
	global_store_dword v39, v64, s[20:21] sc1
	global_store_dword v39, v65, s[22:23] sc1
	global_store_dword v39, v66, s[24:25] sc1
	global_store_dword v39, v67, s[26:27] sc1
	s_add_u32 s20, s20, 0x80000
	s_addc_u32 s21, s21, 0
	s_add_u32 s22, s22, 0x80000
	s_addc_u32 s23, s23, 0
	s_add_u32 s24, s24, 0x80000
	s_addc_u32 s25, s25, 0
	s_add_u32 s26, s26, 0x80000
	s_addc_u32 s27, s27, 0
	global_store_dword v39, v68, s[20:21] sc1
	global_store_dword v39, v69, s[22:23] sc1
	global_store_dword v39, v70, s[24:25] sc1
	global_store_dword v39, v71, s[26:27] sc1
	s_add_u32 s20, s20, 0x80000
	s_addc_u32 s21, s21, 0
	s_add_u32 s22, s22, 0x80000
	s_addc_u32 s23, s23, 0
	s_add_u32 s24, s24, 0x80000
	s_addc_u32 s25, s25, 0
	s_add_u32 s26, s26, 0x80000
	s_addc_u32 s27, s27, 0
	global_store_dword v39, v72, s[20:21] sc1
	global_store_dword v39, v73, s[22:23] sc1
	global_store_dword v39, v74, s[24:25] sc1
	global_store_dword v39, v75, s[26:27] sc1
	s_add_u32 s20, s20, 0x80000
	s_addc_u32 s21, s21, 0
	s_add_u32 s22, s22, 0x80000
	s_addc_u32 s23, s23, 0
	s_add_u32 s24, s24, 0x80000
	s_addc_u32 s25, s25, 0
	s_add_u32 s26, s26, 0x80000
	s_addc_u32 s27, s27, 0
	global_store_dword v39, v76, s[20:21] sc1
	global_store_dword v39, v77, s[22:23] sc1
	global_store_dword v39, v78, s[24:25] sc1
	global_store_dword v39, v79, s[26:27] sc1
	s_add_u32 s20, s20, 0x80000
	s_addc_u32 s21, s21, 0
	s_add_u32 s22, s22, 0x80000
	s_addc_u32 s23, s23, 0
	s_add_u32 s24, s24, 0x80000
	s_addc_u32 s25, s25, 0
	s_add_u32 s26, s26, 0x80000
	s_addc_u32 s27, s27, 0
	global_store_dword v39, v80, s[20:21] sc1
	global_store_dword v39, v81, s[22:23] sc1
	global_store_dword v39, v82, s[24:25] sc1
	global_store_dword v39, v83, s[26:27] sc1
	s_add_u32 s20, s20, 0x80000
	s_addc_u32 s21, s21, 0
	s_add_u32 s22, s22, 0x80000
	s_addc_u32 s23, s23, 0
	s_add_u32 s24, s24, 0x80000
	s_addc_u32 s25, s25, 0
	s_add_u32 s26, s26, 0x80000
	s_addc_u32 s27, s27, 0
	global_store_dword v39, v84, s[20:21] sc1
	global_store_dword v39, v85, s[22:23] sc1
	global_store_dword v39, v86, s[24:25] sc1
	global_store_dword v39, v87, s[26:27] sc1
	s_add_u32 s20, s20, 0x80000
	s_addc_u32 s21, s21, 0
	s_add_u32 s22, s22, 0x80000
	s_addc_u32 s23, s23, 0
	s_add_u32 s24, s24, 0x80000
	s_addc_u32 s25, s25, 0
	s_add_u32 s26, s26, 0x80000
	s_addc_u32 s27, s27, 0
	global_store_dword v39, v88, s[20:21] sc1
	global_store_dword v39, v89, s[22:23] sc1
	global_store_dword v39, v90, s[24:25] sc1
	global_store_dword v39, v91, s[26:27] sc1
	s_add_u32 s20, s20, 0x80000
	s_addc_u32 s21, s21, 0
	s_add_u32 s22, s22, 0x80000
	s_addc_u32 s23, s23, 0
	s_add_u32 s24, s24, 0x80000
	s_addc_u32 s25, s25, 0
	s_add_u32 s26, s26, 0x80000
	s_addc_u32 s27, s27, 0
	global_store_dword v39, v92, s[20:21] sc1
	global_store_dword v39, v93, s[22:23] sc1
	global_store_dword v39, v94, s[24:25] sc1
	global_store_dword v39, v95, s[26:27] sc1
	s_add_u32 s20, s20, 0x80000
	s_addc_u32 s21, s21, 0
	s_add_u32 s22, s22, 0x80000
	s_addc_u32 s23, s23, 0
	s_add_u32 s24, s24, 0x80000
	s_addc_u32 s25, s25, 0
	s_add_u32 s26, s26, 0x80000
	s_addc_u32 s27, s27, 0
	global_store_dword v39, v96, s[20:21] sc1
	global_store_dword v39, v97, s[22:23] sc1
	global_store_dword v39, v98, s[24:25] sc1
	global_store_dword v39, v99, s[26:27] sc1
	s_add_u32 s20, s20, 0x80000
	s_addc_u32 s21, s21, 0
	s_add_u32 s22, s22, 0x80000
	s_addc_u32 s23, s23, 0
	s_add_u32 s24, s24, 0x80000
	s_addc_u32 s25, s25, 0
	s_add_u32 s26, s26, 0x80000
	s_addc_u32 s27, s27, 0
	global_store_dword v39, v100, s[20:21] sc1
	global_store_dword v39, v101, s[22:23] sc1
	global_store_dword v39, v102, s[24:25] sc1
	global_store_dword v39, v103, s[26:27] sc1
	s_add_u32 s20, s20, 0x80000
	s_addc_u32 s21, s21, 0
	s_add_u32 s22, s22, 0x80000
	s_addc_u32 s23, s23, 0
	s_add_u32 s24, s24, 0x80000
	s_addc_u32 s25, s25, 0
	s_add_u32 s26, s26, 0x80000
	s_addc_u32 s27, s27, 0
	global_store_dword v39, v104, s[20:21] sc1
	global_store_dword v39, v105, s[22:23] sc1
	global_store_dword v39, v106, s[24:25] sc1
	global_store_dword v39, v107, s[26:27] sc1
	s_add_u32 s20, s20, 0x80000
	s_addc_u32 s21, s21, 0
	s_add_u32 s22, s22, 0x80000
	s_addc_u32 s23, s23, 0
	s_add_u32 s24, s24, 0x80000
	s_addc_u32 s25, s25, 0
	s_add_u32 s26, s26, 0x80000
	s_addc_u32 s27, s27, 0
	global_store_dword v39, v108, s[20:21] sc1
	global_store_dword v39, v109, s[22:23] sc1
	global_store_dword v39, v110, s[24:25] sc1
	global_store_dword v39, v111, s[26:27] sc1
	s_add_u32 s20, s20, 0x80000
	s_addc_u32 s21, s21, 0
	s_add_u32 s22, s22, 0x80000
	s_addc_u32 s23, s23, 0
	s_add_u32 s24, s24, 0x80000
	s_addc_u32 s25, s25, 0
	s_add_u32 s26, s26, 0x80000
	s_addc_u32 s27, s27, 0
	global_store_dword v39, v112, s[20:21] sc1
	global_store_dword v39, v113, s[22:23] sc1
	global_store_dword v39, v114, s[24:25] sc1
	global_store_dword v39, v115, s[26:27] sc1
	s_add_u32 s20, s20, 0x80000
	s_addc_u32 s21, s21, 0
	s_add_u32 s22, s22, 0x80000
	s_addc_u32 s23, s23, 0
	s_add_u32 s24, s24, 0x80000
	s_addc_u32 s25, s25, 0
	s_add_u32 s26, s26, 0x80000
	s_addc_u32 s27, s27, 0
	global_store_dword v39, v116, s[20:21] sc1
	global_store_dword v39, v117, s[22:23] sc1
	global_store_dword v39, v118, s[24:25] sc1
	global_store_dword v39, v119, s[26:27] sc1
	s_add_u32 s20, s20, 0x80000
	s_addc_u32 s21, s21, 0
	s_add_u32 s22, s22, 0x80000
	s_addc_u32 s23, s23, 0
	s_add_u32 s24, s24, 0x80000
	s_addc_u32 s25, s25, 0
	s_add_u32 s26, s26, 0x80000
	s_addc_u32 s27, s27, 0
	global_store_dword v39, v120, s[20:21] sc1
	global_store_dword v39, v121, s[22:23] sc1
	global_store_dword v39, v122, s[24:25] sc1
	global_store_dword v39, v123, s[26:27] sc1
	s_add_u32 s20, s20, 0x80000
	s_addc_u32 s21, s21, 0
	s_add_u32 s22, s22, 0x80000
	s_addc_u32 s23, s23, 0
	s_add_u32 s24, s24, 0x80000
	s_addc_u32 s25, s25, 0
	s_add_u32 s26, s26, 0x80000
	s_addc_u32 s27, s27, 0
	global_store_dword v39, v124, s[20:21] sc1
	global_store_dword v39, v125, s[22:23] sc1
	global_store_dword v39, v126, s[24:25] sc1
	global_store_dword v39, v127, s[26:27] sc1
	v_mul_f32_e32 v40, 0x3c010204, v40
	v_and_b32_e32 v42, 63, v0
	v_lshlrev_b32_e32 v41, 14, v42
	s_mov_b32 s15, s12
	s_lshl_b32 s15, s15, 2
	s_add_u32 s8, s8, s15
	s_addc_u32 s9, s9, 0
	s_add_u32 s15, s29, 24
	v_cmp_gt_u32_e32 vcc, s15, v42
	s_and_saveexec_b64 s[38:39], vcc
	global_store_dword v41, v40, s[8:9]
	s_mov_b64 exec, s[38:39]
	s_lshl_b32 s15, s14, 12
	v_add_u32_e32 v41, s15, v34
	s_barrier
	ds_write_b128 v41, v[2:5]
	ds_write_b128 v41, v[6:9] offset:1024
	ds_write_b128 v41, v[10:13] offset:2048
	ds_write_b128 v41, v[14:17] offset:3072
	s_waitcnt lgkmcnt(0)
	s_barrier
	s_movk_i32 s15, 0x100
	v_cmp_gt_u32_e32 vcc, s15, v0
	s_and_saveexec_b64 s[38:39], vcc
	s_cbranch_execz .Lk1_end
	v_lshlrev_b32_e32 v16, 4, v0
	ds_read_b128 v[2:5], v16
	ds_read_b128 v[18:21], v16 offset:4096
	ds_read_b128 v[22:25], v16 offset:8192
	ds_read_b128 v[26:29], v16 offset:12288
	ds_read_b128 v[30:33], v16 offset:16384
	ds_read_b128 v[34:37], v16 offset:20480
	ds_read_b128 v[38:41], v16 offset:24576
	ds_read_b128 v[42:45], v16 offset:28672
	s_waitcnt lgkmcnt(6)
	v_pk_add_f32 v[2:3], v[2:3], v[18:19]
	v_pk_add_f32 v[4:5], v[4:5], v[20:21]
	s_waitcnt lgkmcnt(5)
	v_pk_add_f32 v[2:3], v[2:3], v[22:23]
	v_pk_add_f32 v[4:5], v[4:5], v[24:25]
	s_waitcnt lgkmcnt(4)
	v_pk_add_f32 v[2:3], v[2:3], v[26:27]
	v_pk_add_f32 v[4:5], v[4:5], v[28:29]
	s_waitcnt lgkmcnt(3)
	v_pk_add_f32 v[2:3], v[2:3], v[30:31]
	v_pk_add_f32 v[4:5], v[4:5], v[32:33]
	s_waitcnt lgkmcnt(2)
	v_pk_add_f32 v[2:3], v[2:3], v[34:35]
	v_pk_add_f32 v[4:5], v[4:5], v[36:37]
	s_waitcnt lgkmcnt(1)
	v_pk_add_f32 v[2:3], v[2:3], v[38:39]
	v_pk_add_f32 v[4:5], v[4:5], v[40:41]
	s_waitcnt lgkmcnt(0)
	v_pk_add_f32 v[2:3], v[2:3], v[42:43]
	v_pk_add_f32 v[4:5], v[4:5], v[44:45]
	s_lshl_b32 s15, s2, 12
	s_add_u32 s10, s10, s15
	s_addc_u32 s11, s11, 0
	global_store_dwordx4 v16, v[2:5], s[10:11]
